# v33 with a lower outstanding-load cap in the phase-1 prologue (vmcnt 24)
# speedup vs baseline: 1.0036x; 1.0036x over previous
; __device__ __forceinline__ unsigned cvt_pk_bf16(float lo, float hi) { unsigned r; asm volatile("v_cvt_pk_bf16_f32 %0, %1, %2" : "=v"(r) : "v"(lo), "v"(hi)); return r; }
; #define GAS __attribute__((address_space(1)))
; #define LAS __attribute__((address_space(3)))
; __device__ __forceinline__ void conv_load(const ConvSrc& c, int lane, f32x4 (&ra)[8], f32x4 (&rb)[8]) {
;     const int nblk = c.N >> 6, kb = c.kfast ? (c.item & 31) : c.item / nblk, nb = c.kfast ? (c.item >> 5) : c.item - kb * nblk, k0 = kb * 64, n0 = nb * 64;
;     const int n4 = (lane & 15) * 4, kq = lane >> 4;
; #pragma unroll
;     for (int i = 0; i < 8; ++i) { const int kp2 = 4 * i + kq; const float* p = c.W + (size_t)(k0 + 2 * kp2) * c.N + n0 + n4; ra[i] = __builtin_nontemporal_load((const GAS f32x4*)p); rb[i] = __builtin_nontemporal_load((const GAS f32x4*)(p + c.N)); }
; }
; __device__ __forceinline__ void conv_emit(const ConvSrc& c, int lane, LAS unsigned* P, const f32x4 (&ra)[8], const f32x4 (&rb)[8]) {
;     const int nblk = c.N >> 6, kb = c.kfast ? (c.item & 31) : c.item / nblk, nb = c.kfast ? (c.item >> 5) : c.item - kb * nblk, k0 = kb * 64, n0 = nb * 64;
;     const int n4 = (lane & 15) * 4, kq = lane >> 4;
; #pragma unroll
;     for (int i = 0; i < 8; ++i) { const int kp2 = 4 * i + kq; LAS unsigned* d = P + kp2 * 65 + n4;
;         d[0] = pg8::cvt_pk_bf16(ra[i].x, rb[i].x); d[1] = pg8::cvt_pk_bf16(ra[i].y, rb[i].y); d[2] = pg8::cvt_pk_bf16(ra[i].z, rb[i].z); d[3] = pg8::cvt_pk_bf16(ra[i].w, rb[i].w); }
.LBB0_30:
	s_lshr_b32 s4, s2, 6
	v_cvt_f32_u32_e32 v0, s4
	s_sub_i32 s34, 0, s4
	s_abs_i32 s29, s17
	s_ashr_i32 s21, s17, 31
	v_rcp_iflag_f32_e32 v0, v0
	v_mov_b32_e32 v131, v129
	v_mul_f32_e32 v0, 0x4f7ffffe, v0
	v_cvt_u32_f32_e32 v0, v0
	s_nop 0
	v_readfirstlane_b32 s35, v0
	s_mul_i32 s34, s34, s35
	s_mul_hi_u32 s34, s35, s34
	s_add_i32 s35, s35, s34
	s_mul_hi_u32 s34, s29, s35
	s_mul_i32 s35, s34, s4
	s_sub_i32 s29, s29, s35
	s_add_i32 s36, s34, 1
	s_sub_i32 s35, s29, s4
	s_cmp_ge_u32 s29, s4
	s_cselect_b32 s34, s36, s34
	s_cselect_b32 s29, s35, s29
	s_add_i32 s35, s34, 1
	s_cmp_ge_u32 s29, s4
	s_cselect_b32 s29, s35, s34
	s_xor_b32 s29, s29, s21
	s_sub_i32 s21, s29, s21
	v_lshl_add_u32 v28, s21, 6, v133
	s_mul_i32 s4, s21, s4
	v_mad_u64_u32 v[0:1], s[34:35], v28, s2, 0
	s_sub_i32 s4, s17, s4
	v_ashrrev_i32_e32 v3, 31, v28
	v_mov_b32_e32 v2, v1
	s_lshl_b32 s34, s4, 6
	v_mad_u64_u32 v[2:3], s[36:37], v3, s2, v[2:3]
	s_ashr_i32 s35, s34, 31
	v_mov_b32_e32 v1, v2
	s_waitcnt lgkmcnt(0)
	v_lshl_add_u64 v[0:1], v[0:1], 2, s[30:31]
	s_lshl_b64 s[34:35], s[34:35], 2
	v_lshl_add_u64 v[0:1], v[0:1], 0, s[34:35]
	v_lshl_add_u64 v[0:1], v[0:1], 0, v[128:129]
	s_lshl_b64 s[36:37], s[2:3], 2
	v_lshl_add_u64 v[4:5], v[0:1], 0, s[36:37]
	global_load_dwordx4 v[0:3], v[0:1], off nt
	s_nop 0
	global_load_dwordx4 v[32:35], v[4:5], off nt
	v_add_u32_e32 v4, 8, v28
	v_ashrrev_i32_e32 v7, 31, v4
	v_mad_u64_u32 v[4:5], s[44:45], v4, s2, 0
	v_mov_b32_e32 v6, v5
	v_mad_u64_u32 v[6:7], s[44:45], v7, s2, v[6:7]
	v_mov_b32_e32 v5, v6
	v_lshl_add_u64 v[4:5], v[4:5], 2, s[30:31]
	v_lshl_add_u64 v[4:5], v[4:5], 0, s[34:35]
	v_lshl_add_u64 v[4:5], v[4:5], 0, v[128:129]
	v_lshl_add_u64 v[8:9], v[4:5], 0, s[36:37]
	global_load_dwordx4 v[4:7], v[4:5], off nt
	s_nop 0
	global_load_dwordx4 v[44:47], v[8:9], off nt
	v_add_u32_e32 v8, 16, v28
	v_ashrrev_i32_e32 v11, 31, v8
	v_mad_u64_u32 v[8:9], s[44:45], v8, s2, 0
	v_mov_b32_e32 v10, v9
	v_mad_u64_u32 v[10:11], s[44:45], v11, s2, v[10:11]
	v_mov_b32_e32 v9, v10
	v_lshl_add_u64 v[8:9], v[8:9], 2, s[30:31]
	v_lshl_add_u64 v[8:9], v[8:9], 0, s[34:35]
	v_lshl_add_u64 v[8:9], v[8:9], 0, v[128:129]
	v_lshl_add_u64 v[12:13], v[8:9], 0, s[36:37]
	global_load_dwordx4 v[8:11], v[8:9], off nt
	s_nop 0
	global_load_dwordx4 v[48:51], v[12:13], off nt
	v_add_u32_e32 v12, 24, v28
	v_ashrrev_i32_e32 v15, 31, v12
	v_mad_u64_u32 v[12:13], s[44:45], v12, s2, 0
	v_mov_b32_e32 v14, v13
	v_mad_u64_u32 v[14:15], s[44:45], v15, s2, v[14:15]
	v_mov_b32_e32 v13, v14
	v_lshl_add_u64 v[12:13], v[12:13], 2, s[30:31]
	v_lshl_add_u64 v[12:13], v[12:13], 0, s[34:35]
	v_lshl_add_u64 v[12:13], v[12:13], 0, v[128:129]
	v_lshl_add_u64 v[16:17], v[12:13], 0, s[36:37]
	global_load_dwordx4 v[12:15], v[12:13], off nt
	s_nop 0
	global_load_dwordx4 v[52:55], v[16:17], off nt
	v_add_u32_e32 v16, 32, v28
	v_ashrrev_i32_e32 v19, 31, v16
	v_mad_u64_u32 v[16:17], s[44:45], v16, s2, 0
	v_mov_b32_e32 v18, v17
	v_mad_u64_u32 v[18:19], s[44:45], v19, s2, v[18:19]
	v_mov_b32_e32 v17, v18
	v_lshl_add_u64 v[16:17], v[16:17], 2, s[30:31]
	v_lshl_add_u64 v[16:17], v[16:17], 0, s[34:35]
	v_lshl_add_u64 v[16:17], v[16:17], 0, v[128:129]
	v_lshl_add_u64 v[20:21], v[16:17], 0, s[36:37]
	global_load_dwordx4 v[16:19], v[16:17], off nt
	s_nop 0
	global_load_dwordx4 v[56:59], v[20:21], off nt
	v_add_u32_e32 v20, 40, v28
	v_ashrrev_i32_e32 v23, 31, v20
	v_mad_u64_u32 v[20:21], s[44:45], v20, s2, 0
	v_mov_b32_e32 v22, v21
	v_mad_u64_u32 v[22:23], s[44:45], v23, s2, v[22:23]
	v_mov_b32_e32 v21, v22
	v_lshl_add_u64 v[20:21], v[20:21], 2, s[30:31]
	v_lshl_add_u64 v[20:21], v[20:21], 0, s[34:35]
	v_lshl_add_u64 v[20:21], v[20:21], 0, v[128:129]
	v_lshl_add_u64 v[24:25], v[20:21], 0, s[36:37]
	global_load_dwordx4 v[20:23], v[20:21], off nt
	s_nop 0
	global_load_dwordx4 v[60:63], v[24:25], off nt
	v_add_u32_e32 v24, 48, v28
	v_ashrrev_i32_e32 v27, 31, v24
	v_mad_u64_u32 v[24:25], s[44:45], v24, s2, 0
	v_mov_b32_e32 v26, v25
	v_mad_u64_u32 v[26:27], s[44:45], v27, s2, v[26:27]
	v_mov_b32_e32 v25, v26
	v_lshl_add_u64 v[24:25], v[24:25], 2, s[30:31]
	v_lshl_add_u64 v[24:25], v[24:25], 0, s[34:35]
	v_lshl_add_u64 v[24:25], v[24:25], 0, v[128:129]
	v_lshl_add_u64 v[26:27], v[24:25], 0, s[36:37]
	global_load_dwordx4 v[36:39], v[24:25], off nt
	global_load_dwordx4 v[40:43], v[26:27], off nt
	v_add_u32_e32 v24, 56, v28
	v_ashrrev_i32_e32 v27, 31, v24
	v_mad_u64_u32 v[24:25], s[44:45], v24, s2, 0
	v_mov_b32_e32 v26, v25
	v_mad_u64_u32 v[26:27], s[44:45], v27, s2, v[26:27]
	v_mov_b32_e32 v25, v26
	v_lshl_add_u64 v[24:25], v[24:25], 2, s[30:31]
	v_lshl_add_u64 v[24:25], v[24:25], 0, s[34:35]
	v_lshl_add_u64 v[24:25], v[24:25], 0, v[128:129]
	v_lshl_add_u64 v[26:27], v[24:25], 0, s[36:37]
	global_load_dwordx4 v[28:31], v[24:25], off nt
	s_nop 0
	global_load_dwordx4 v[24:27], v[26:27], off nt
	s_waitcnt vmcnt(38)
	v_cvt_pk_bf16_f32 v120, v120, v124
	ds_write_b32 v140, v120
	v_cvt_pk_bf16_f32 v120, v121, v125
	ds_write_b32 v140, v120 offset:4
	v_cvt_pk_bf16_f32 v120, v122, v126
	ds_write_b32 v140, v120 offset:8
	v_cvt_pk_bf16_f32 v120, v123, v127
	ds_write_b32 v140, v120 offset:12
	s_waitcnt vmcnt(36)
	v_cvt_pk_bf16_f32 v112, v112, v116
	ds_write_b32 v140, v112 offset:1040
	v_cvt_pk_bf16_f32 v112, v113, v117
	ds_write_b32 v140, v112 offset:1044
	v_cvt_pk_bf16_f32 v112, v114, v118
	ds_write_b32 v140, v112 offset:1048
	v_cvt_pk_bf16_f32 v112, v115, v119
	ds_write_b32 v140, v112 offset:1052
	s_waitcnt vmcnt(34)
; __device__ __forceinline__ unsigned cvt_pk_bf16(float lo, float hi) { unsigned r; asm volatile("v_cvt_pk_bf16_f32 %0, %1, %2" : "=v"(r) : "v"(lo), "v"(hi)); return r; }
; #define GAS __attribute__((address_space(1)))
; #define LAS __attribute__((address_space(3)))
; #define LDS_WAIT() asm volatile("s_waitcnt lgkmcnt(0)" ::: "memory")
; __device__ __forceinline__ void conv_emit(const ConvSrc& c, int lane, LAS unsigned* P, const f32x4 (&ra)[8], const f32x4 (&rb)[8]) {
;     ...
;     for (int i = 0; i < 8; ++i) { const int kp2 = 4 * i + kq; LAS unsigned* d = P + kp2 * 65 + n4;
;         d[0] = pg8::cvt_pk_bf16(ra[i].x, rb[i].x); d[1] = pg8::cvt_pk_bf16(ra[i].y, rb[i].y); d[2] = pg8::cvt_pk_bf16(ra[i].z, rb[i].z); d[3] = pg8::cvt_pk_bf16(ra[i].w, rb[i].w); }
;     LDS_WAIT(); asm volatile("" ::: "memory");
;     const int cc = lane & 7;
; #pragma unroll
;     for (int jj = 0; jj < 8; ++jj) { const int n = (lane >> 3) + 8 * jj; const LAS unsigned* sp = P + (4 * cc) * 65 + n;
;         v4u o; o.x = sp[0]; o.y = sp[65]; o.z = sp[130]; o.w = sp[195];
;         bf16* dst = c.tiled ? c.WT + (size_t)((nb >> 2) * c.tiled + c.ktoff + kb) * 16384 + ((nb & 3) * 64 + n) * 64 + 8 * cc : c.WT + (size_t)(n0 + n) * c.ldk + k0 + 8 * cc;
;         __builtin_nontemporal_store(o, (GAS v4u*)dst); }
;     LDS_WAIT(); asm volatile("" ::: "memory");
	v_cvt_pk_bf16_f32 v104, v104, v108
	ds_write_b32 v140, v104 offset:2080
	v_cvt_pk_bf16_f32 v104, v105, v109
	ds_write_b32 v140, v104 offset:2084
	v_cvt_pk_bf16_f32 v104, v106, v110
	ds_write_b32 v140, v104 offset:2088
	v_cvt_pk_bf16_f32 v104, v107, v111
	ds_write_b32 v140, v104 offset:2092
	s_waitcnt vmcnt(32)
	v_cvt_pk_bf16_f32 v96, v96, v100
	ds_write_b32 v140, v96 offset:3120
	v_cvt_pk_bf16_f32 v96, v97, v101
	ds_write_b32 v140, v96 offset:3124
	v_cvt_pk_bf16_f32 v96, v98, v102
	ds_write_b32 v140, v96 offset:3128
	v_cvt_pk_bf16_f32 v96, v99, v103
	ds_write_b32 v140, v96 offset:3132
	s_waitcnt vmcnt(24)
	v_cvt_pk_bf16_f32 v88, v88, v92
	ds_write_b32 v140, v88 offset:4160
	v_cvt_pk_bf16_f32 v88, v89, v93
	ds_write_b32 v140, v88 offset:4164
	v_cvt_pk_bf16_f32 v88, v90, v94
	ds_write_b32 v140, v88 offset:4168
	v_cvt_pk_bf16_f32 v88, v91, v95
	ds_write_b32 v140, v88 offset:4172
	s_waitcnt vmcnt(28)
	v_cvt_pk_bf16_f32 v80, v80, v84
	ds_write_b32 v140, v80 offset:5200
	v_cvt_pk_bf16_f32 v80, v81, v85
	ds_write_b32 v140, v80 offset:5204
	v_cvt_pk_bf16_f32 v80, v82, v86
	ds_write_b32 v140, v80 offset:5208
	v_cvt_pk_bf16_f32 v80, v83, v87
	ds_write_b32 v140, v80 offset:5212
	s_waitcnt vmcnt(26)
	v_cvt_pk_bf16_f32 v72, v72, v76
	ds_write_b32 v140, v72 offset:6240
	v_cvt_pk_bf16_f32 v72, v73, v77
	ds_write_b32 v140, v72 offset:6244
	v_cvt_pk_bf16_f32 v72, v74, v78
	ds_write_b32 v140, v72 offset:6248
	v_cvt_pk_bf16_f32 v72, v75, v79
	ds_write_b32 v140, v72 offset:6252
	s_waitcnt vmcnt(24)
	v_cvt_pk_bf16_f32 v64, v64, v68
	ds_write_b32 v140, v64 offset:7280
	v_cvt_pk_bf16_f32 v64, v65, v69
	ds_write_b32 v140, v64 offset:7284
	v_cvt_pk_bf16_f32 v64, v66, v70
	ds_write_b32 v140, v64 offset:7288
	v_cvt_pk_bf16_f32 v64, v67, v71
	ds_write_b32 v140, v64 offset:7292
	s_ashr_i32 s4, s43, 2
	s_waitcnt lgkmcnt(0)
	s_mul_i32 s4, s4, s42
	s_add_i32 s5, s20, s5
	s_add_i32 s4, s5, s4
	ds_read2_b32 v[72:73], v134 offset1:8
	ds_read2_b32 v[64:65], v134 offset0:65 offset1:73
	ds_read2_b32 v[74:75], v134 offset0:130 offset1:138
	ds_read2_b32 v[66:67], v134 offset0:195 offset1:203
	s_ashr_i32 s5, s4, 31
	s_and_b32 s21, s28, 0xc0
	s_lshl_b64 s[4:5], s[4:5], 15
	s_add_u32 s26, s26, s4
	v_add_lshl_u32 v76, s21, v132, 6
	s_addc_u32 s27, s27, s5
	v_ashrrev_i32_e32 v77, 31, v76
	v_lshl_add_u64 v[76:77], v[76:77], 1, s[26:27]
	s_waitcnt lgkmcnt(3)
	v_mov_b32_e32 v68, v72
	s_waitcnt lgkmcnt(2)
	v_mov_b32_e32 v69, v64
	s_waitcnt lgkmcnt(1)
	v_mov_b32_e32 v70, v74
	s_waitcnt lgkmcnt(0)
	v_mov_b32_e32 v71, v66
	v_lshl_add_u64 v[76:77], v[76:77], 0, v[130:131]
	global_store_dwordx4 v[76:77], v[68:71], off nt
	v_mov_b32_e32 v64, v73
	v_mov_b32_e32 v66, v75
	v_add_lshl_u32 v68, s21, v135, 6
	v_ashrrev_i32_e32 v69, 31, v68
	v_lshl_add_u64 v[68:69], v[68:69], 1, s[26:27]
	v_lshl_add_u64 v[72:73], v[68:69], 0, v[130:131]
	ds_read2_b32 v[74:75], v134 offset0:16 offset1:24
	ds_read2_b32 v[68:69], v134 offset0:81 offset1:89
	ds_read2_b32 v[76:77], v134 offset0:146 offset1:154
	ds_read2_b32 v[70:71], v134 offset0:211 offset1:219
	global_store_dwordx4 v[72:73], v[64:67], off nt
	v_add_lshl_u32 v72, s21, v136, 6
	v_ashrrev_i32_e32 v73, 31, v72
	v_lshl_add_u64 v[72:73], v[72:73], 1, s[26:27]
	s_waitcnt lgkmcnt(3)
	v_mov_b32_e32 v64, v74
	s_waitcnt lgkmcnt(2)
	v_mov_b32_e32 v65, v68
	s_waitcnt lgkmcnt(1)
	v_mov_b32_e32 v66, v76
	s_waitcnt lgkmcnt(0)
	v_mov_b32_e32 v67, v70
	v_lshl_add_u64 v[72:73], v[72:73], 0, v[130:131]
	global_store_dwordx4 v[72:73], v[64:67], off nt
	v_mov_b32_e32 v68, v75
	v_mov_b32_e32 v70, v77
	v_add_lshl_u32 v64, s21, v137, 6
	v_ashrrev_i32_e32 v65, 31, v64
	v_lshl_add_u64 v[64:65], v[64:65], 1, s[26:27]
	v_lshl_add_u64 v[72:73], v[64:65], 0, v[130:131]
	ds_read2_b32 v[74:75], v134 offset0:32 offset1:40
	ds_read2_b32 v[64:65], v134 offset0:97 offset1:105
	ds_read2_b32 v[76:77], v134 offset0:162 offset1:170
	ds_read2_b32 v[66:67], v134 offset0:227 offset1:235
	global_store_dwordx4 v[72:73], v[68:71], off nt
	v_add_lshl_u32 v72, s21, v138, 6
	v_ashrrev_i32_e32 v73, 31, v72
	v_lshl_add_u64 v[72:73], v[72:73], 1, s[26:27]
	s_waitcnt lgkmcnt(3)
	v_mov_b32_e32 v68, v74
	s_waitcnt lgkmcnt(2)
	v_mov_b32_e32 v69, v64
	s_waitcnt lgkmcnt(1)
	v_mov_b32_e32 v70, v76
	s_waitcnt lgkmcnt(0)
	v_mov_b32_e32 v71, v66
	v_lshl_add_u64 v[72:73], v[72:73], 0, v[130:131]
	global_store_dwordx4 v[72:73], v[68:71], off nt
	v_mov_b32_e32 v64, v75
	v_mov_b32_e32 v66, v77
	v_add_lshl_u32 v68, s21, v139, 6
	v_ashrrev_i32_e32 v69, 31, v68
	v_lshl_add_u64 v[68:69], v[68:69], 1, s[26:27]
	v_lshl_add_u64 v[72:73], v[68:69], 0, v[130:131]
	ds_read2_b32 v[74:75], v134 offset0:48 offset1:56
	ds_read2_b32 v[68:69], v134 offset0:113 offset1:121
	ds_read2_b32 v[76:77], v134 offset0:178 offset1:186
	ds_read2_b32 v[70:71], v134 offset0:243 offset1:251
	global_store_dwordx4 v[72:73], v[64:67], off nt
	v_add_lshl_u32 v72, s21, v141, 6
	v_ashrrev_i32_e32 v73, 31, v72
	v_lshl_add_u64 v[72:73], v[72:73], 1, s[26:27]
	s_waitcnt lgkmcnt(3)
	v_mov_b32_e32 v64, v74
	s_waitcnt lgkmcnt(2)
	v_mov_b32_e32 v65, v68
	s_waitcnt lgkmcnt(1)
	v_mov_b32_e32 v66, v76
	s_waitcnt lgkmcnt(0)
	v_mov_b32_e32 v67, v70
	v_lshl_add_u64 v[72:73], v[72:73], 0, v[130:131]
	global_store_dwordx4 v[72:73], v[64:67], off nt
	v_mov_b32_e32 v68, v75
	v_mov_b32_e32 v70, v77
	v_add_lshl_u32 v64, s21, v142, 6
	v_ashrrev_i32_e32 v65, 31, v64
	v_lshl_add_u64 v[64:65], v[64:65], 1, s[26:27]
	v_lshl_add_u64 v[64:65], v[64:65], 0, v[130:131]
	global_store_dwordx4 v[64:65], v[68:71], off nt
	s_waitcnt lgkmcnt(0)
	s_cmpk_gt_i32 s22, 0x2bff
	s_mov_b32 s21, s2
	s_cbranch_scc1 .LBB0_71

; __device__ __forceinline__ void phase1(KP kp, LAS unsigned char* lds, int wave, int bid, int G) {
;     ...
;     for (int c = tid; c < 2048; c += 512) { float sh = b_ada[c], sc = b_ada[2048 + c];
;         for (int r = 0; r < 16; ++r) { sh += modp[r * 12288 + c]; sc += modp[r * 12288 + 2048 + c]; }
;         A1[c] = n1g[c] * (1.0f + sc); B1[c] = sh; }
.LBB0_125:
	v_ashrrev_i32_e32 v7, 31, v2
	v_mov_b32_e32 v6, v2
	v_lshlrev_b64 v[12:13], 2, v[6:7]
	v_ashrrev_i32_e32 v5, 31, v3
	v_mov_b32_e32 v4, v3
	v_lshl_add_u64 v[10:11], s[8:9], 0, v[12:13]
	v_lshlrev_b64 v[14:15], 2, v[4:5]
	s_waitcnt vmcnt(8)
	v_add_co_u32_e32 v24, vcc, s5, v10
	v_lshl_add_u64 v[8:9], s[8:9], 0, v[14:15]
	v_lshl_add_u64 v[6:7], s[26:27], 0, v[12:13]
	v_lshl_add_u64 v[18:19], s[10:11], 0, v[12:13]
	v_addc_co_u32_e32 v25, vcc, 0, v11, vcc
	v_lshl_add_u64 v[4:5], s[26:27], 0, v[14:15]
	v_lshl_add_u64 v[16:17], s[10:11], 0, v[14:15]
	global_load_dword v12, v[10:11], off
	global_load_dword v13, v[8:9], off
	global_load_dword v14, v[6:7], off
	global_load_dword v15, v[4:5], off
	s_nop 0
	global_load_dword v10, v[18:19], off
	v_add_co_u32_e32 v18, vcc, s5, v8
	v_add_u32_e32 v23, -2, v23
	s_nop 0
	v_addc_co_u32_e32 v19, vcc, 0, v9, vcc
	v_add_co_u32_e32 v26, vcc, s5, v6
	global_load_dword v8, v[24:25], off
	global_load_dword v9, v[18:19], off
	v_addc_co_u32_e32 v27, vcc, 0, v7, vcc
	v_add_co_u32_e32 v24, vcc, s5, v4
	v_add_u32_e32 v3, 0x400, v3
	s_nop 0
	v_addc_co_u32_e32 v25, vcc, 0, v5, vcc
	v_add_co_u32_e32 v28, vcc, s17, v6
	global_load_dword v18, v[26:27], off
	global_load_dword v19, v[24:25], off
	v_addc_co_u32_e32 v29, vcc, 0, v7, vcc
	v_add_co_u32_e32 v24, vcc, s17, v4
	v_add_u32_e32 v2, 0x400, v2
	s_nop 0
	v_addc_co_u32_e32 v25, vcc, 0, v5, vcc
	v_add_co_u32_e32 v26, vcc, s18, v6
	global_load_dword v28, v[28:29], off
	s_nop 0
	global_load_dword v29, v[24:25], off
	v_addc_co_u32_e32 v27, vcc, 0, v7, vcc
	v_add_co_u32_e32 v24, vcc, s18, v4
	v_addc_co_u32_e32 v25, vcc, 0, v5, vcc
	v_add_co_u32_e32 v30, vcc, s19, v6
	global_load_dword v26, v[26:27], off
	s_nop 0
	global_load_dword v27, v[24:25], off
	v_addc_co_u32_e32 v31, vcc, 0, v7, vcc
	v_add_co_u32_e32 v24, vcc, s19, v4
	v_addc_co_u32_e32 v25, vcc, 0, v5, vcc
	v_add_co_u32_e32 v32, vcc, s20, v6
	global_load_dword v30, v[30:31], off
	s_nop 0
	global_load_dword v31, v[24:25], off
	v_addc_co_u32_e32 v33, vcc, 0, v7, vcc
	v_add_co_u32_e32 v24, vcc, s20, v4
	s_nop 1
	v_addc_co_u32_e32 v25, vcc, 0, v5, vcc
	v_add_co_u32_e32 v34, vcc, s21, v6
	global_load_dword v32, v[32:33], off
	s_nop 0
	global_load_dword v33, v[24:25], off
	v_addc_co_u32_e32 v35, vcc, 0, v7, vcc
	v_add_co_u32_e32 v24, vcc, s21, v4
	v_addc_co_u32_e32 v25, vcc, 0, v5, vcc
	v_add_co_u32_e32 v36, vcc, s22, v6
	global_load_dword v34, v[34:35], off
	s_nop 0
	global_load_dword v35, v[24:25], off
	v_addc_co_u32_e32 v37, vcc, 0, v7, vcc
	v_add_co_u32_e32 v24, vcc, s22, v4
	s_nop 1
	v_addc_co_u32_e32 v25, vcc, 0, v5, vcc
	v_add_co_u32_e32 v38, vcc, s23, v6
	global_load_dword v36, v[36:37], off
	s_nop 0
	global_load_dword v37, v[24:25], off
	v_addc_co_u32_e32 v39, vcc, 0, v7, vcc
	v_add_co_u32_e32 v24, vcc, s23, v4
	v_addc_co_u32_e32 v25, vcc, 0, v5, vcc
	v_add_co_u32_e32 v40, vcc, s24, v6
	global_load_dword v38, v[38:39], off
	s_nop 0
	global_load_dword v39, v[24:25], off
	v_addc_co_u32_e32 v41, vcc, 0, v7, vcc
	v_add_co_u32_e32 v24, vcc, s24, v4
	s_nop 1
	v_addc_co_u32_e32 v25, vcc, 0, v5, vcc
	v_add_co_u32_e32 v42, vcc, s25, v6
	global_load_dword v40, v[40:41], off
	s_nop 0
	global_load_dword v41, v[24:25], off
	v_addc_co_u32_e32 v43, vcc, 0, v7, vcc
	v_add_co_u32_e32 v24, vcc, s25, v4
	v_addc_co_u32_e32 v25, vcc, 0, v5, vcc
	v_add_co_u32_e32 v44, vcc, s30, v6
	global_load_dword v42, v[42:43], off
	s_nop 0
	global_load_dword v43, v[24:25], off
	v_addc_co_u32_e32 v45, vcc, 0, v7, vcc
	v_add_co_u32_e32 v24, vcc, s30, v4
	s_nop 1
	v_addc_co_u32_e32 v25, vcc, 0, v5, vcc
	v_add_co_u32_e32 v46, vcc, s31, v6
	global_load_dword v44, v[44:45], off
	s_nop 0
	global_load_dword v45, v[24:25], off
	v_addc_co_u32_e32 v47, vcc, 0, v7, vcc
	v_add_co_u32_e32 v24, vcc, s31, v4
	v_addc_co_u32_e32 v25, vcc, 0, v5, vcc
	v_add_co_u32_e32 v48, vcc, s34, v6
	global_load_dword v46, v[46:47], off
	s_nop 0
	global_load_dword v47, v[24:25], off
	v_addc_co_u32_e32 v49, vcc, 0, v7, vcc
	v_add_co_u32_e32 v24, vcc, s34, v4
	s_nop 1
	v_addc_co_u32_e32 v25, vcc, 0, v5, vcc
	v_add_co_u32_e32 v50, vcc, s35, v6
	global_load_dword v48, v[48:49], off
	s_nop 0
	global_load_dword v49, v[24:25], off
	v_addc_co_u32_e32 v51, vcc, 0, v7, vcc
	v_add_co_u32_e32 v24, vcc, s35, v4
	v_addc_co_u32_e32 v25, vcc, 0, v5, vcc
	v_add_co_u32_e32 v52, vcc, s36, v6
	global_load_dword v50, v[50:51], off
	s_nop 0
	global_load_dword v51, v[24:25], off
	v_addc_co_u32_e32 v53, vcc, 0, v7, vcc
	v_add_co_u32_e32 v24, vcc, s36, v4
	s_nop 1
	v_addc_co_u32_e32 v25, vcc, 0, v5, vcc
	v_add_co_u32_e32 v54, vcc, s37, v6
	global_load_dword v52, v[52:53], off
	s_nop 0
	global_load_dword v53, v[24:25], off
	v_addc_co_u32_e32 v55, vcc, 0, v7, vcc
	v_add_co_u32_e32 v24, vcc, s37, v4
	s_waitcnt vmcnt(24)
; __device__ __forceinline__ void phase1(KP kp, LAS unsigned char* lds, int wave, int bid, int G) {
;     ...
;     for (int c = tid; c < 2048; c += 512) { float sh = b_ada[c], sc = b_ada[2048 + c];
;         for (int r = 0; r < 16; ++r) { sh += modp[r * 12288 + c]; sc += modp[r * 12288 + 2048 + c]; }
;         A1[c] = n1g[c] * (1.0f + sc); B1[c] = sh; }
	v_addc_co_u32_e32 v25, vcc, 0, v5, vcc
	v_add_co_u32_e32 v56, vcc, s38, v6
	global_load_dword v54, v[54:55], off
	s_nop 0
	global_load_dword v55, v[24:25], off
	v_addc_co_u32_e32 v57, vcc, 0, v7, vcc
	v_add_co_u32_e32 v24, vcc, s38, v4
	s_nop 1
	v_addc_co_u32_e32 v25, vcc, 0, v5, vcc
	v_add_co_u32_e32 v58, vcc, s39, v6
	global_load_dword v56, v[56:57], off
	s_nop 0
	global_load_dword v57, v[24:25], off
	v_addc_co_u32_e32 v59, vcc, 0, v7, vcc
	v_add_co_u32_e32 v24, vcc, s39, v4
	v_addc_co_u32_e32 v25, vcc, 0, v5, vcc
	v_add_co_u32_e32 v60, vcc, s40, v6
	global_load_dword v58, v[58:59], off
	s_nop 0
	global_load_dword v59, v[24:25], off
	v_addc_co_u32_e32 v61, vcc, 0, v7, vcc
	v_add_co_u32_e32 v24, vcc, s40, v4
	s_nop 1
	v_addc_co_u32_e32 v25, vcc, 0, v5, vcc
	v_add_co_u32_e32 v62, vcc, s41, v6
	global_load_dword v60, v[60:61], off
	s_nop 0
	global_load_dword v61, v[24:25], off
	v_addc_co_u32_e32 v63, vcc, 0, v7, vcc
	v_add_co_u32_e32 v24, vcc, s41, v4
	v_addc_co_u32_e32 v25, vcc, 0, v5, vcc
	v_add_co_u32_e32 v66, vcc, s42, v6
	global_load_dword v62, v[62:63], off
	s_nop 0
	global_load_dword v63, v[24:25], off
	v_addc_co_u32_e32 v67, vcc, 0, v7, vcc
	v_add_co_u32_e32 v24, vcc, s42, v4
	s_nop 1
	v_addc_co_u32_e32 v25, vcc, 0, v5, vcc
	v_add_co_u32_e32 v68, vcc, s43, v6
	global_load_dword v66, v[66:67], off
	s_nop 0
	global_load_dword v67, v[24:25], off
	v_addc_co_u32_e32 v69, vcc, 0, v7, vcc
	v_add_co_u32_e32 v24, vcc, s43, v4
	v_addc_co_u32_e32 v25, vcc, 0, v5, vcc
	v_add_co_u32_e32 v70, vcc, s44, v6
	global_load_dword v68, v[68:69], off
	s_nop 0
	global_load_dword v69, v[24:25], off
	v_addc_co_u32_e32 v71, vcc, 0, v7, vcc
	v_add_co_u32_e32 v24, vcc, s44, v4
	s_nop 1
	v_addc_co_u32_e32 v25, vcc, 0, v5, vcc
	v_add_co_u32_e32 v72, vcc, s45, v6
	global_load_dword v70, v[70:71], off
	s_nop 0
	global_load_dword v71, v[24:25], off
	v_addc_co_u32_e32 v73, vcc, 0, v7, vcc
	v_add_co_u32_e32 v24, vcc, s45, v4
	v_addc_co_u32_e32 v25, vcc, 0, v5, vcc
	v_add_co_u32_e32 v74, vcc, s46, v6
	global_load_dword v72, v[72:73], off
	s_nop 0
	global_load_dword v73, v[24:25], off
	v_addc_co_u32_e32 v75, vcc, 0, v7, vcc
	v_add_co_u32_e32 v24, vcc, s46, v4
	s_nop 1
	v_addc_co_u32_e32 v25, vcc, 0, v5, vcc
	v_add_co_u32_e32 v76, vcc, s47, v6
	global_load_dword v74, v[74:75], off
	s_nop 0
	global_load_dword v75, v[24:25], off
	v_addc_co_u32_e32 v77, vcc, 0, v7, vcc
	v_add_co_u32_e32 v24, vcc, s47, v4
	v_addc_co_u32_e32 v25, vcc, 0, v5, vcc
	v_add_co_u32_e32 v78, vcc, s48, v6
	global_load_dword v76, v[76:77], off
	s_nop 0
	global_load_dword v77, v[24:25], off
	v_addc_co_u32_e32 v79, vcc, 0, v7, vcc
	v_add_co_u32_e32 v24, vcc, s48, v4
	s_nop 1
	v_addc_co_u32_e32 v25, vcc, 0, v5, vcc
	v_add_co_u32_e32 v80, vcc, s49, v6
	global_load_dword v78, v[78:79], off
	s_nop 0
	global_load_dword v79, v[24:25], off
	v_addc_co_u32_e32 v81, vcc, 0, v7, vcc
	v_add_co_u32_e32 v24, vcc, s49, v4
	v_addc_co_u32_e32 v25, vcc, 0, v5, vcc
	v_add_co_u32_e32 v82, vcc, s50, v6
	global_load_dword v80, v[80:81], off
	s_nop 0
	global_load_dword v81, v[24:25], off
	v_addc_co_u32_e32 v83, vcc, 0, v7, vcc
	v_add_co_u32_e32 v24, vcc, s50, v4
	s_nop 1
	v_addc_co_u32_e32 v25, vcc, 0, v5, vcc
	v_add_co_u32_e32 v84, vcc, s51, v6
	global_load_dword v82, v[82:83], off
	s_nop 0
	global_load_dword v83, v[24:25], off
	v_addc_co_u32_e32 v85, vcc, 0, v7, vcc
	v_add_co_u32_e32 v24, vcc, s51, v4
	v_addc_co_u32_e32 v25, vcc, 0, v5, vcc
	v_add_co_u32_e32 v6, vcc, s52, v6
	global_load_dword v84, v[84:85], off
	s_nop 0
	global_load_dword v85, v[24:25], off
	v_addc_co_u32_e32 v7, vcc, 0, v7, vcc
	v_add_co_u32_e32 v4, vcc, s52, v4
	s_nop 1
	v_addc_co_u32_e32 v5, vcc, 0, v5, vcc
	global_load_dword v6, v[6:7], off
	s_nop 0
	global_load_dword v7, v[4:5], off
	global_load_dword v11, v[16:17], off
	s_waitcnt vmcnt(5)
	v_pk_add_f32 v[8:9], v[8:9], v[18:19]
	s_nop 0
	v_pk_add_f32 v[8:9], v[8:9], v[26:27]
	s_nop 0
	v_pk_add_f32 v[8:9], v[8:9], v[32:33]
	s_nop 0
	v_pk_add_f32 v[8:9], v[8:9], v[36:37]
	s_nop 0
	v_pk_add_f32 v[8:9], v[8:9], v[40:41]
	s_nop 0
	v_pk_add_f32 v[8:9], v[8:9], v[44:45]
	s_nop 0
	v_pk_add_f32 v[8:9], v[8:9], v[48:49]
	s_nop 0
	v_pk_add_f32 v[8:9], v[8:9], v[52:53]
	s_nop 0
	v_pk_add_f32 v[8:9], v[8:9], v[56:57]
	s_nop 0
	v_pk_add_f32 v[8:9], v[8:9], v[60:61]
	s_nop 0
	v_pk_add_f32 v[8:9], v[8:9], v[66:67]
	s_nop 0
	v_pk_add_f32 v[8:9], v[8:9], v[70:71]
	s_nop 0
	v_pk_add_f32 v[8:9], v[8:9], v[74:75]
	s_nop 0
	v_pk_add_f32 v[8:9], v[8:9], v[78:79]
	s_nop 0
	v_pk_add_f32 v[8:9], v[8:9], v[82:83]
	s_nop 0
	v_pk_add_f32 v[4:5], v[12:13], v[14:15]
	v_cmp_eq_u32_e32 vcc, 0, v23
	v_pk_add_f32 v[4:5], v[4:5], v[28:29]
	s_or_b64 s[28:29], vcc, s[28:29]
	v_pk_add_f32 v[4:5], v[4:5], v[30:31]
	s_nop 0
	v_pk_add_f32 v[4:5], v[4:5], v[34:35]
	s_nop 0
	v_pk_add_f32 v[4:5], v[4:5], v[38:39]
	s_nop 0
	v_pk_add_f32 v[4:5], v[4:5], v[42:43]
	s_nop 0
	v_pk_add_f32 v[4:5], v[4:5], v[46:47]
	s_nop 0
	v_pk_add_f32 v[4:5], v[4:5], v[50:51]
	s_nop 0
	v_pk_add_f32 v[4:5], v[4:5], v[54:55]
	s_nop 0
	v_pk_add_f32 v[4:5], v[4:5], v[58:59]
	s_nop 0
	v_pk_add_f32 v[4:5], v[4:5], v[62:63]
	s_nop 0
	v_pk_add_f32 v[4:5], v[4:5], v[68:69]
	s_nop 0
	v_pk_add_f32 v[4:5], v[4:5], v[72:73]
	s_nop 0
	v_pk_add_f32 v[4:5], v[4:5], v[76:77]
	s_nop 0
	v_pk_add_f32 v[4:5], v[4:5], v[80:81]
	s_waitcnt vmcnt(3)
	v_pk_add_f32 v[4:5], v[4:5], v[84:85]
	ds_write2st64_b32 v22, v4, v5 offset0:32 offset1:40
	s_waitcnt vmcnt(1)
	v_pk_add_f32 v[4:5], v[8:9], v[6:7]
	s_nop 0
	v_pk_add_f32 v[4:5], v[4:5], 1.0 op_sel_hi:[1,0]
	s_waitcnt vmcnt(0)
	v_pk_mul_f32 v[4:5], v[10:11], v[4:5]
	ds_write2st64_b32 v22, v4, v5 offset1:8
	v_add_u32_e32 v22, 0x1000, v22
	s_andn2_b64 exec, exec, s[28:29]
	s_cbranch_execnz .LBB0_125
	s_or_b64 exec, exec, s[28:29]
	v_cmp_ne_u32_e32 vcc, v20, v21
	v_lshl_add_u32 v2, v21, 9, v0
	s_orn2_b64 s[26:27], vcc, exec

; __device__ __forceinline__ unsigned cvt_pk_bf16(float lo, float hi) { unsigned r; asm volatile("v_cvt_pk_bf16_f32 %0, %1, %2" : "=v"(r) : "v"(lo), "v"(hi)); return r; }
; #define GAS __attribute__((address_space(1)))
; #define LAS __attribute__((address_space(3)))
; __device__ __forceinline__ void conv_load(const ConvSrc& c, int lane, f32x4 (&ra)[8], f32x4 (&rb)[8]) {
;     const int nblk = c.N >> 6, kb = c.kfast ? (c.item & 31) : c.item / nblk, nb = c.kfast ? (c.item >> 5) : c.item - kb * nblk, k0 = kb * 64, n0 = nb * 64;
;     const int n4 = (lane & 15) * 4, kq = lane >> 4;
; #pragma unroll
;     for (int i = 0; i < 8; ++i) { const int kp2 = 4 * i + kq; const float* p = c.W + (size_t)(k0 + 2 * kp2) * c.N + n0 + n4; ra[i] = __builtin_nontemporal_load((const GAS f32x4*)p); rb[i] = __builtin_nontemporal_load((const GAS f32x4*)(p + c.N)); }
; }
; __device__ __forceinline__ void conv_emit(const ConvSrc& c, int lane, LAS unsigned* P, const f32x4 (&ra)[8], const f32x4 (&rb)[8]) {
;     const int nblk = c.N >> 6, kb = c.kfast ? (c.item & 31) : c.item / nblk, nb = c.kfast ? (c.item >> 5) : c.item - kb * nblk, k0 = kb * 64, n0 = nb * 64;
;     const int n4 = (lane & 15) * 4, kq = lane >> 4;
; #pragma unroll
;     for (int i = 0; i < 8; ++i) { const int kp2 = 4 * i + kq; LAS unsigned* d = P + kp2 * 65 + n4;
;         d[0] = pg8::cvt_pk_bf16(ra[i].x, rb[i].x); d[1] = pg8::cvt_pk_bf16(ra[i].y, rb[i].y); d[2] = pg8::cvt_pk_bf16(ra[i].z, rb[i].z); d[3] = pg8::cvt_pk_bf16(ra[i].w, rb[i].w); }
.LBB0_614:
	s_lshr_b32 s4, s6, 6
	v_cvt_f32_u32_e32 v2, s4
	s_sub_i32 s63, 0, s4
	s_abs_i32 s62, s69
	s_ashr_i32 s59, s69, 31
	v_rcp_iflag_f32_e32 v2, v2
	v_mov_b32_e32 v135, v1
	v_mul_f32_e32 v2, 0x4f7ffffe, v2
	v_cvt_u32_f32_e32 v2, v2
	s_nop 0
	v_readfirstlane_b32 s64, v2
	s_mul_i32 s63, s63, s64
	s_mul_hi_u32 s63, s64, s63
	s_add_i32 s64, s64, s63
	s_mul_hi_u32 s63, s62, s64
	s_mul_i32 s64, s63, s4
	s_sub_i32 s62, s62, s64
	s_add_i32 s65, s63, 1
	s_sub_i32 s64, s62, s4
	s_cmp_ge_u32 s62, s4
	s_cselect_b32 s63, s65, s63
	s_cselect_b32 s62, s64, s62
	s_add_i32 s64, s63, 1
	s_cmp_ge_u32 s62, s4
	s_cselect_b32 s62, s64, s63
	s_xor_b32 s62, s62, s59
	s_sub_i32 s59, s62, s59
	v_lshl_add_u32 v52, s59, 6, v133
	s_mul_i32 s4, s59, s4
	v_mad_u64_u32 v[2:3], s[62:63], v52, s6, 0
	s_sub_i32 s4, s69, s4
	v_ashrrev_i32_e32 v5, 31, v52
	v_mov_b32_e32 v4, v3
	s_lshl_b32 s62, s4, 6
	v_mad_u64_u32 v[4:5], s[64:65], v5, s6, v[4:5]
	s_ashr_i32 s63, s62, 31
	v_mov_b32_e32 v3, v4
	s_waitcnt lgkmcnt(0)
	v_lshl_add_u64 v[2:3], v[2:3], 2, s[60:61]
	s_lshl_b64 s[62:63], s[62:63], 2
	v_lshl_add_u64 v[2:3], v[2:3], 0, s[62:63]
	v_lshl_add_u64 v[2:3], v[2:3], 0, v[0:1]
	s_lshl_b64 s[64:65], s[6:7], 2
	v_lshl_add_u64 v[6:7], v[2:3], 0, s[64:65]
	global_load_dwordx4 v[2:5], v[2:3], off nt
	s_nop 0
	global_load_dwordx4 v[26:29], v[6:7], off nt
	v_add_u32_e32 v6, 8, v52
	v_ashrrev_i32_e32 v9, 31, v6
	v_mad_u64_u32 v[6:7], vcc, v6, s6, 0
	v_mov_b32_e32 v8, v7
	v_mad_u64_u32 v[8:9], vcc, v9, s6, v[8:9]
	v_mov_b32_e32 v7, v8
	v_lshl_add_u64 v[6:7], v[6:7], 2, s[60:61]
	v_lshl_add_u64 v[6:7], v[6:7], 0, s[62:63]
	v_lshl_add_u64 v[6:7], v[6:7], 0, v[0:1]
	v_lshl_add_u64 v[10:11], v[6:7], 0, s[64:65]
	global_load_dwordx4 v[6:9], v[6:7], off nt
	s_nop 0
	global_load_dwordx4 v[34:37], v[10:11], off nt
	v_add_u32_e32 v10, 16, v52
	v_ashrrev_i32_e32 v13, 31, v10
	v_mad_u64_u32 v[10:11], vcc, v10, s6, 0
	v_mov_b32_e32 v12, v11
	v_mad_u64_u32 v[12:13], vcc, v13, s6, v[12:13]
	v_mov_b32_e32 v11, v12
	v_lshl_add_u64 v[10:11], v[10:11], 2, s[60:61]
	v_lshl_add_u64 v[10:11], v[10:11], 0, s[62:63]
	v_lshl_add_u64 v[10:11], v[10:11], 0, v[0:1]
	v_lshl_add_u64 v[14:15], v[10:11], 0, s[64:65]
	global_load_dwordx4 v[10:13], v[10:11], off nt
	s_nop 0
	global_load_dwordx4 v[30:33], v[14:15], off nt
	v_add_u32_e32 v14, 24, v52
	v_ashrrev_i32_e32 v17, 31, v14
	v_mad_u64_u32 v[14:15], vcc, v14, s6, 0
	v_mov_b32_e32 v16, v15
	v_mad_u64_u32 v[16:17], vcc, v17, s6, v[16:17]
	v_mov_b32_e32 v15, v16
	v_lshl_add_u64 v[14:15], v[14:15], 2, s[60:61]
	v_lshl_add_u64 v[14:15], v[14:15], 0, s[62:63]
	v_lshl_add_u64 v[14:15], v[14:15], 0, v[0:1]
	v_lshl_add_u64 v[18:19], v[14:15], 0, s[64:65]
	global_load_dwordx4 v[14:17], v[14:15], off nt
	s_nop 0
	global_load_dwordx4 v[42:45], v[18:19], off nt
	v_add_u32_e32 v18, 32, v52
	v_ashrrev_i32_e32 v21, 31, v18
	v_mad_u64_u32 v[18:19], vcc, v18, s6, 0
	v_mov_b32_e32 v20, v19
	v_mad_u64_u32 v[20:21], vcc, v21, s6, v[20:21]
	v_mov_b32_e32 v19, v20
	v_lshl_add_u64 v[18:19], v[18:19], 2, s[60:61]
	v_lshl_add_u64 v[18:19], v[18:19], 0, s[62:63]
	v_lshl_add_u64 v[18:19], v[18:19], 0, v[0:1]
	v_lshl_add_u64 v[22:23], v[18:19], 0, s[64:65]
	global_load_dwordx4 v[18:21], v[18:19], off nt
	s_nop 0
	global_load_dwordx4 v[38:41], v[22:23], off nt
	v_add_u32_e32 v22, 40, v52
	v_ashrrev_i32_e32 v25, 31, v22
	v_mad_u64_u32 v[22:23], vcc, v22, s6, 0
	v_mov_b32_e32 v24, v23
	v_mad_u64_u32 v[24:25], vcc, v25, s6, v[24:25]
	v_mov_b32_e32 v23, v24
	v_lshl_add_u64 v[22:23], v[22:23], 2, s[60:61]
	v_lshl_add_u64 v[22:23], v[22:23], 0, s[62:63]
	v_lshl_add_u64 v[22:23], v[22:23], 0, v[0:1]
	v_lshl_add_u64 v[46:47], v[22:23], 0, s[64:65]
	global_load_dwordx4 v[22:25], v[22:23], off nt
	s_nop 0
	global_load_dwordx4 v[62:65], v[46:47], off nt
	v_add_u32_e32 v46, 48, v52
	v_ashrrev_i32_e32 v49, 31, v46
	v_mad_u64_u32 v[46:47], vcc, v46, s6, 0
	v_mov_b32_e32 v48, v47
	v_mad_u64_u32 v[48:49], vcc, v49, s6, v[48:49]
	v_mov_b32_e32 v47, v48
	v_lshl_add_u64 v[46:47], v[46:47], 2, s[60:61]
	v_lshl_add_u64 v[46:47], v[46:47], 0, s[62:63]
	v_lshl_add_u64 v[46:47], v[46:47], 0, v[0:1]
	v_lshl_add_u64 v[50:51], v[46:47], 0, s[64:65]
	global_load_dwordx4 v[46:49], v[46:47], off nt
	s_nop 0
	global_load_dwordx4 v[58:61], v[50:51], off nt
	v_add_u32_e32 v50, 56, v52
	v_ashrrev_i32_e32 v53, 31, v50
	v_mad_u64_u32 v[50:51], vcc, v50, s6, 0
	v_mov_b32_e32 v52, v51
	v_mad_u64_u32 v[52:53], vcc, v53, s6, v[52:53]
	v_mov_b32_e32 v51, v52
	v_lshl_add_u64 v[50:51], v[50:51], 2, s[60:61]
	v_lshl_add_u64 v[50:51], v[50:51], 0, s[62:63]
	v_lshl_add_u64 v[50:51], v[50:51], 0, v[0:1]
	v_lshl_add_u64 v[52:53], v[50:51], 0, s[64:65]
	global_load_dwordx4 v[54:57], v[50:51], off nt
	s_nop 0
	global_load_dwordx4 v[50:53], v[52:53], off nt
	s_waitcnt vmcnt(38)
	v_cvt_pk_bf16_f32 v0, v66, v74
	ds_write_b32 v144, v0
	v_cvt_pk_bf16_f32 v0, v67, v75
	ds_write_b32 v144, v0 offset:4
	v_cvt_pk_bf16_f32 v0, v68, v76
	ds_write_b32 v144, v0 offset:8
	v_cvt_pk_bf16_f32 v0, v69, v77
	ds_write_b32 v144, v0 offset:12
	s_waitcnt vmcnt(36)
	v_cvt_pk_bf16_f32 v0, v70, v82
	ds_write_b32 v144, v0 offset:1040
	v_cvt_pk_bf16_f32 v0, v71, v83
	ds_write_b32 v144, v0 offset:1044
	v_cvt_pk_bf16_f32 v0, v72, v84
	ds_write_b32 v144, v0 offset:1048
	v_cvt_pk_bf16_f32 v0, v73, v85
	ds_write_b32 v144, v0 offset:1052
	s_waitcnt vmcnt(34)
; __device__ __forceinline__ unsigned cvt_pk_bf16(float lo, float hi) { unsigned r; asm volatile("v_cvt_pk_bf16_f32 %0, %1, %2" : "=v"(r) : "v"(lo), "v"(hi)); return r; }
; #define GAS __attribute__((address_space(1)))
; #define LAS __attribute__((address_space(3)))
; #define LDS_WAIT() asm volatile("s_waitcnt lgkmcnt(0)" ::: "memory")
; __device__ __forceinline__ void conv_emit(const ConvSrc& c, int lane, LAS unsigned* P, const f32x4 (&ra)[8], const f32x4 (&rb)[8]) {
;     ...
;     for (int i = 0; i < 8; ++i) { const int kp2 = 4 * i + kq; LAS unsigned* d = P + kp2 * 65 + n4;
;         d[0] = pg8::cvt_pk_bf16(ra[i].x, rb[i].x); d[1] = pg8::cvt_pk_bf16(ra[i].y, rb[i].y); d[2] = pg8::cvt_pk_bf16(ra[i].z, rb[i].z); d[3] = pg8::cvt_pk_bf16(ra[i].w, rb[i].w); }
;     LDS_WAIT(); asm volatile("" ::: "memory");
;     const int cc = lane & 7;
; #pragma unroll
;     for (int jj = 0; jj < 8; ++jj) { const int n = (lane >> 3) + 8 * jj; const LAS unsigned* sp = P + (4 * cc) * 65 + n;
;         v4u o; o.x = sp[0]; o.y = sp[65]; o.z = sp[130]; o.w = sp[195];
;         bf16* dst = c.tiled ? c.WT + (size_t)((nb >> 2) * c.tiled + c.ktoff + kb) * 16384 + ((nb & 3) * 64 + n) * 64 + 8 * cc : c.WT + (size_t)(n0 + n) * c.ldk + k0 + 8 * cc;
;         __builtin_nontemporal_store(o, (GAS v4u*)dst); }
;     LDS_WAIT(); asm volatile("" ::: "memory");
	v_cvt_pk_bf16_f32 v0, v78, v90
	ds_write_b32 v144, v0 offset:2080
	v_cvt_pk_bf16_f32 v0, v79, v91
	ds_write_b32 v144, v0 offset:2084
	v_cvt_pk_bf16_f32 v0, v80, v92
	ds_write_b32 v144, v0 offset:2088
	v_cvt_pk_bf16_f32 v0, v81, v93
	ds_write_b32 v144, v0 offset:2092
	s_waitcnt vmcnt(32)
	v_cvt_pk_bf16_f32 v0, v86, v98
	ds_write_b32 v144, v0 offset:3120
	v_cvt_pk_bf16_f32 v0, v87, v99
	ds_write_b32 v144, v0 offset:3124
	v_cvt_pk_bf16_f32 v0, v88, v100
	ds_write_b32 v144, v0 offset:3128
	v_cvt_pk_bf16_f32 v0, v89, v101
	ds_write_b32 v144, v0 offset:3132
	s_waitcnt vmcnt(24)
	v_cvt_pk_bf16_f32 v0, v94, v106
	ds_write_b32 v144, v0 offset:4160
	v_cvt_pk_bf16_f32 v0, v95, v107
	ds_write_b32 v144, v0 offset:4164
	v_cvt_pk_bf16_f32 v0, v96, v108
	ds_write_b32 v144, v0 offset:4168
	v_cvt_pk_bf16_f32 v0, v97, v109
	ds_write_b32 v144, v0 offset:4172
	s_waitcnt vmcnt(28)
	v_cvt_pk_bf16_f32 v0, v102, v114
	ds_write_b32 v144, v0 offset:5200
	v_cvt_pk_bf16_f32 v0, v103, v115
	ds_write_b32 v144, v0 offset:5204
	v_cvt_pk_bf16_f32 v0, v104, v116
	ds_write_b32 v144, v0 offset:5208
	v_cvt_pk_bf16_f32 v0, v105, v117
	ds_write_b32 v144, v0 offset:5212
	s_waitcnt vmcnt(26)
	v_cvt_pk_bf16_f32 v0, v110, v126
	ds_write_b32 v144, v0 offset:6240
	v_cvt_pk_bf16_f32 v0, v111, v127
	ds_write_b32 v144, v0 offset:6244
	v_cvt_pk_bf16_f32 v0, v112, v128
	ds_write_b32 v144, v0 offset:6248
	v_cvt_pk_bf16_f32 v0, v113, v129
	ds_write_b32 v144, v0 offset:6252
	s_waitcnt vmcnt(24)
	v_cvt_pk_bf16_f32 v0, v118, v122
	ds_write_b32 v144, v0 offset:7280
	v_cvt_pk_bf16_f32 v0, v119, v123
	ds_write_b32 v144, v0 offset:7284
	v_cvt_pk_bf16_f32 v0, v120, v124
	ds_write_b32 v144, v0 offset:7288
	v_cvt_pk_bf16_f32 v0, v121, v125
	ds_write_b32 v144, v0 offset:7292
	s_ashr_i32 s4, s21, 2
	s_waitcnt lgkmcnt(0)
	s_mul_i32 s4, s4, s5
	s_add_i32 s5, s20, s19
	s_add_i32 s4, s5, s4
	ds_read2_b32 v[74:75], v136 offset1:8
	ds_read2_b32 v[66:67], v136 offset0:65 offset1:73
	ds_read2_b32 v[76:77], v136 offset0:130 offset1:138
	ds_read2_b32 v[68:69], v136 offset0:195 offset1:203
	s_ashr_i32 s5, s4, 31
	s_and_b32 s21, s58, 0xc0
	s_lshl_b64 s[4:5], s[4:5], 15
	s_add_u32 s56, s56, s4
	v_add_lshl_u32 v78, s21, v131, 6
	s_addc_u32 s57, s57, s5
	v_ashrrev_i32_e32 v79, 31, v78
	v_lshl_add_u64 v[78:79], v[78:79], 1, s[56:57]
	s_waitcnt lgkmcnt(3)
	v_mov_b32_e32 v70, v74
	s_waitcnt lgkmcnt(2)
	v_mov_b32_e32 v71, v66
	s_waitcnt lgkmcnt(1)
	v_mov_b32_e32 v72, v76
	s_waitcnt lgkmcnt(0)
	v_mov_b32_e32 v73, v68
	v_lshl_add_u64 v[78:79], v[78:79], 0, v[134:135]
	global_store_dwordx4 v[78:79], v[70:73], off nt
	v_mov_b32_e32 v66, v75
	v_mov_b32_e32 v68, v77
	v_add_lshl_u32 v70, s21, v137, 6
	v_ashrrev_i32_e32 v71, 31, v70
	v_lshl_add_u64 v[70:71], v[70:71], 1, s[56:57]
	v_lshl_add_u64 v[74:75], v[70:71], 0, v[134:135]
	ds_read2_b32 v[76:77], v136 offset0:16 offset1:24
	ds_read2_b32 v[70:71], v136 offset0:81 offset1:89
	ds_read2_b32 v[78:79], v136 offset0:146 offset1:154
	ds_read2_b32 v[72:73], v136 offset0:211 offset1:219
	global_store_dwordx4 v[74:75], v[66:69], off nt
	v_add_lshl_u32 v74, s21, v138, 6
	v_ashrrev_i32_e32 v75, 31, v74
	v_lshl_add_u64 v[74:75], v[74:75], 1, s[56:57]
	s_waitcnt lgkmcnt(3)
	v_mov_b32_e32 v66, v76
	s_waitcnt lgkmcnt(2)
	v_mov_b32_e32 v67, v70
	s_waitcnt lgkmcnt(1)
	v_mov_b32_e32 v68, v78
	s_waitcnt lgkmcnt(0)
	v_mov_b32_e32 v69, v72
	v_lshl_add_u64 v[74:75], v[74:75], 0, v[134:135]
	global_store_dwordx4 v[74:75], v[66:69], off nt
	v_mov_b32_e32 v70, v77
	v_mov_b32_e32 v72, v79
	v_add_lshl_u32 v66, s21, v139, 6
	v_ashrrev_i32_e32 v67, 31, v66
	v_lshl_add_u64 v[66:67], v[66:67], 1, s[56:57]
	v_lshl_add_u64 v[74:75], v[66:67], 0, v[134:135]
	ds_read2_b32 v[76:77], v136 offset0:32 offset1:40
	ds_read2_b32 v[66:67], v136 offset0:97 offset1:105
	ds_read2_b32 v[78:79], v136 offset0:162 offset1:170
	ds_read2_b32 v[68:69], v136 offset0:227 offset1:235
	global_store_dwordx4 v[74:75], v[70:73], off nt
	v_add_lshl_u32 v74, s21, v140, 6
	v_ashrrev_i32_e32 v75, 31, v74
	v_lshl_add_u64 v[74:75], v[74:75], 1, s[56:57]
	s_waitcnt lgkmcnt(3)
	v_mov_b32_e32 v70, v76
	s_waitcnt lgkmcnt(2)
	v_mov_b32_e32 v71, v66
	s_waitcnt lgkmcnt(1)
	v_mov_b32_e32 v72, v78
	s_waitcnt lgkmcnt(0)
	v_mov_b32_e32 v73, v68
	v_lshl_add_u64 v[74:75], v[74:75], 0, v[134:135]
	global_store_dwordx4 v[74:75], v[70:73], off nt
	v_mov_b32_e32 v66, v77
	v_mov_b32_e32 v68, v79
	v_add_lshl_u32 v70, s21, v141, 6
	v_ashrrev_i32_e32 v71, 31, v70
	v_lshl_add_u64 v[70:71], v[70:71], 1, s[56:57]
	v_lshl_add_u64 v[74:75], v[70:71], 0, v[134:135]
	ds_read2_b32 v[76:77], v136 offset0:48 offset1:56
	ds_read2_b32 v[70:71], v136 offset0:113 offset1:121
	ds_read2_b32 v[78:79], v136 offset0:178 offset1:186
	ds_read2_b32 v[72:73], v136 offset0:243 offset1:251
	global_store_dwordx4 v[74:75], v[66:69], off nt
	v_add_lshl_u32 v74, s21, v142, 6
	v_ashrrev_i32_e32 v75, 31, v74
	v_lshl_add_u64 v[74:75], v[74:75], 1, s[56:57]
	s_waitcnt lgkmcnt(3)
	v_mov_b32_e32 v66, v76
	s_waitcnt lgkmcnt(2)
	v_mov_b32_e32 v67, v70
	s_waitcnt lgkmcnt(1)
	v_mov_b32_e32 v68, v78
	s_waitcnt lgkmcnt(0)
	v_mov_b32_e32 v69, v72
	v_lshl_add_u64 v[74:75], v[74:75], 0, v[134:135]
	global_store_dwordx4 v[74:75], v[66:69], off nt
	v_mov_b32_e32 v70, v77
	v_mov_b32_e32 v72, v79
	v_add_lshl_u32 v66, s21, v143, 6
	v_ashrrev_i32_e32 v67, 31, v66
	v_lshl_add_u64 v[66:67], v[66:67], 1, s[56:57]
	v_lshl_add_u64 v[66:67], v[66:67], 0, v[134:135]
	global_store_dwordx4 v[66:67], v[70:73], off nt
	s_waitcnt lgkmcnt(0)
	s_cmp_lt_i32 s23, 0x12c00
	s_mov_b32 s4, s6
	s_cbranch_scc0 .LBB0_321

; __device__ __forceinline__ unsigned cvt_pk_bf16(float lo, float hi) { unsigned r; asm volatile("v_cvt_pk_bf16_f32 %0, %1, %2" : "=v"(r) : "v"(lo), "v"(hi)); return r; }
; #define GAS __attribute__((address_space(1)))
; #define LAS __attribute__((address_space(3)))
; __device__ __forceinline__ void conv_load(const ConvSrc& c, int lane, f32x4 (&ra)[8], f32x4 (&rb)[8]) {
;     const int nblk = c.N >> 6, kb = c.kfast ? (c.item & 31) : c.item / nblk, nb = c.kfast ? (c.item >> 5) : c.item - kb * nblk, k0 = kb * 64, n0 = nb * 64;
;     const int n4 = (lane & 15) * 4, kq = lane >> 4;
; #pragma unroll
;     for (int i = 0; i < 8; ++i) { const int kp2 = 4 * i + kq; const float* p = c.W + (size_t)(k0 + 2 * kp2) * c.N + n0 + n4; ra[i] = __builtin_nontemporal_load((const GAS f32x4*)p); rb[i] = __builtin_nontemporal_load((const GAS f32x4*)(p + c.N)); }
; }
; __device__ __forceinline__ void conv_emit(const ConvSrc& c, int lane, LAS unsigned* P, const f32x4 (&ra)[8], const f32x4 (&rb)[8]) {
;     const int nblk = c.N >> 6, kb = c.kfast ? (c.item & 31) : c.item / nblk, nb = c.kfast ? (c.item >> 5) : c.item - kb * nblk, k0 = kb * 64, n0 = nb * 64;
;     const int n4 = (lane & 15) * 4, kq = lane >> 4;
; #pragma unroll
;     for (int i = 0; i < 8; ++i) { const int kp2 = 4 * i + kq; LAS unsigned* d = P + kp2 * 65 + n4;
;         d[0] = pg8::cvt_pk_bf16(ra[i].x, rb[i].x); d[1] = pg8::cvt_pk_bf16(ra[i].y, rb[i].y); d[2] = pg8::cvt_pk_bf16(ra[i].z, rb[i].z); d[3] = pg8::cvt_pk_bf16(ra[i].w, rb[i].w); }
.LBB0_2247:
	s_lshr_b32 s4, s28, 6
	v_cvt_f32_u32_e32 v0, s4
	s_sub_i32 s47, 0, s4
	s_abs_i32 s46, s18
	s_ashr_i32 s43, s18, 31
	v_rcp_iflag_f32_e32 v0, v0
	v_mov_b32_e32 v131, v129
	v_mul_f32_e32 v0, 0x4f7ffffe, v0
	v_cvt_u32_f32_e32 v0, v0
	s_nop 0
	v_readfirstlane_b32 s48, v0
	s_mul_i32 s47, s47, s48
	s_mul_hi_u32 s47, s48, s47
	s_add_i32 s48, s48, s47
	s_mul_hi_u32 s47, s46, s48
	s_mul_i32 s48, s47, s4
	s_sub_i32 s46, s46, s48
	s_add_i32 s49, s47, 1
	s_sub_i32 s48, s46, s4
	s_cmp_ge_u32 s46, s4
	s_cselect_b32 s47, s49, s47
	s_cselect_b32 s46, s48, s46
	s_add_i32 s48, s47, 1
	s_cmp_ge_u32 s46, s4
	s_cselect_b32 s46, s48, s47
	s_xor_b32 s46, s46, s43
	s_sub_i32 s43, s46, s43
	v_lshl_add_u32 v50, s43, 6, v133
	s_mul_i32 s4, s43, s4
	v_mad_u64_u32 v[0:1], s[46:47], v50, s28, 0
	s_sub_i32 s4, s18, s4
	v_ashrrev_i32_e32 v3, 31, v50
	v_mov_b32_e32 v2, v1
	s_lshl_b32 s46, s4, 6
	v_mad_u64_u32 v[2:3], s[48:49], v3, s28, v[2:3]
	s_ashr_i32 s47, s46, 31
	v_mov_b32_e32 v1, v2
	s_waitcnt lgkmcnt(0)
	v_lshl_add_u64 v[0:1], v[0:1], 2, s[44:45]
	s_lshl_b64 s[46:47], s[46:47], 2
	v_lshl_add_u64 v[0:1], v[0:1], 0, s[46:47]
	v_lshl_add_u64 v[0:1], v[0:1], 0, v[128:129]
	s_lshl_b64 s[48:49], s[28:29], 2
	v_lshl_add_u64 v[4:5], v[0:1], 0, s[48:49]
	global_load_dwordx4 v[0:3], v[0:1], off nt
	s_nop 0
	global_load_dwordx4 v[24:27], v[4:5], off nt
	v_add_u32_e32 v4, 8, v50
	v_ashrrev_i32_e32 v7, 31, v4
	v_mad_u64_u32 v[4:5], s[54:55], v4, s28, 0
	v_mov_b32_e32 v6, v5
	v_mad_u64_u32 v[6:7], s[54:55], v7, s28, v[6:7]
	v_mov_b32_e32 v5, v6
	v_lshl_add_u64 v[4:5], v[4:5], 2, s[44:45]
	v_lshl_add_u64 v[4:5], v[4:5], 0, s[46:47]
	v_lshl_add_u64 v[4:5], v[4:5], 0, v[128:129]
	v_lshl_add_u64 v[8:9], v[4:5], 0, s[48:49]
	global_load_dwordx4 v[4:7], v[4:5], off nt
	s_nop 0
	global_load_dwordx4 v[32:35], v[8:9], off nt
	v_add_u32_e32 v8, 16, v50
	v_ashrrev_i32_e32 v11, 31, v8
	v_mad_u64_u32 v[8:9], s[54:55], v8, s28, 0
	v_mov_b32_e32 v10, v9
	v_mad_u64_u32 v[10:11], s[54:55], v11, s28, v[10:11]
	v_mov_b32_e32 v9, v10
	v_lshl_add_u64 v[8:9], v[8:9], 2, s[44:45]
	v_lshl_add_u64 v[8:9], v[8:9], 0, s[46:47]
	v_lshl_add_u64 v[8:9], v[8:9], 0, v[128:129]
	v_lshl_add_u64 v[12:13], v[8:9], 0, s[48:49]
	global_load_dwordx4 v[8:11], v[8:9], off nt
	s_nop 0
	global_load_dwordx4 v[28:31], v[12:13], off nt
	v_add_u32_e32 v12, 24, v50
	v_ashrrev_i32_e32 v15, 31, v12
	v_mad_u64_u32 v[12:13], s[54:55], v12, s28, 0
	v_mov_b32_e32 v14, v13
	v_mad_u64_u32 v[14:15], s[54:55], v15, s28, v[14:15]
	v_mov_b32_e32 v13, v14
	v_lshl_add_u64 v[12:13], v[12:13], 2, s[44:45]
	v_lshl_add_u64 v[12:13], v[12:13], 0, s[46:47]
	v_lshl_add_u64 v[12:13], v[12:13], 0, v[128:129]
	v_lshl_add_u64 v[16:17], v[12:13], 0, s[48:49]
	global_load_dwordx4 v[12:15], v[12:13], off nt
	s_nop 0
	global_load_dwordx4 v[40:43], v[16:17], off nt
	v_add_u32_e32 v16, 32, v50
	v_ashrrev_i32_e32 v19, 31, v16
	v_mad_u64_u32 v[16:17], s[54:55], v16, s28, 0
	v_mov_b32_e32 v18, v17
	v_mad_u64_u32 v[18:19], s[54:55], v19, s28, v[18:19]
	v_mov_b32_e32 v17, v18
	v_lshl_add_u64 v[16:17], v[16:17], 2, s[44:45]
	v_lshl_add_u64 v[16:17], v[16:17], 0, s[46:47]
	v_lshl_add_u64 v[16:17], v[16:17], 0, v[128:129]
	v_lshl_add_u64 v[20:21], v[16:17], 0, s[48:49]
	global_load_dwordx4 v[16:19], v[16:17], off nt
	s_nop 0
	global_load_dwordx4 v[36:39], v[20:21], off nt
	v_add_u32_e32 v20, 40, v50
	v_ashrrev_i32_e32 v23, 31, v20
	v_mad_u64_u32 v[20:21], s[54:55], v20, s28, 0
	v_mov_b32_e32 v22, v21
	v_mad_u64_u32 v[22:23], s[54:55], v23, s28, v[22:23]
	v_mov_b32_e32 v21, v22
	v_lshl_add_u64 v[20:21], v[20:21], 2, s[44:45]
	v_lshl_add_u64 v[20:21], v[20:21], 0, s[46:47]
	v_lshl_add_u64 v[20:21], v[20:21], 0, v[128:129]
	v_lshl_add_u64 v[44:45], v[20:21], 0, s[48:49]
	global_load_dwordx4 v[20:23], v[20:21], off nt
	s_nop 0
	global_load_dwordx4 v[60:63], v[44:45], off nt
	v_add_u32_e32 v44, 48, v50
	v_ashrrev_i32_e32 v47, 31, v44
	v_mad_u64_u32 v[44:45], s[54:55], v44, s28, 0
	v_mov_b32_e32 v46, v45
	v_mad_u64_u32 v[46:47], s[54:55], v47, s28, v[46:47]
	v_mov_b32_e32 v45, v46
	v_lshl_add_u64 v[44:45], v[44:45], 2, s[44:45]
	v_lshl_add_u64 v[44:45], v[44:45], 0, s[46:47]
	v_lshl_add_u64 v[44:45], v[44:45], 0, v[128:129]
	v_lshl_add_u64 v[48:49], v[44:45], 0, s[48:49]
	global_load_dwordx4 v[44:47], v[44:45], off nt
	s_nop 0
	global_load_dwordx4 v[56:59], v[48:49], off nt
	v_add_u32_e32 v48, 56, v50
	v_ashrrev_i32_e32 v51, 31, v48
	v_mad_u64_u32 v[48:49], s[54:55], v48, s28, 0
	v_mov_b32_e32 v50, v49
	v_mad_u64_u32 v[50:51], s[54:55], v51, s28, v[50:51]
	v_mov_b32_e32 v49, v50
	v_lshl_add_u64 v[48:49], v[48:49], 2, s[44:45]
	v_lshl_add_u64 v[48:49], v[48:49], 0, s[46:47]
	v_lshl_add_u64 v[48:49], v[48:49], 0, v[128:129]
	v_lshl_add_u64 v[50:51], v[48:49], 0, s[48:49]
	global_load_dwordx4 v[52:55], v[48:49], off nt
	s_nop 0
	global_load_dwordx4 v[48:51], v[50:51], off nt
	s_waitcnt vmcnt(38)
	v_cvt_pk_bf16_f32 v64, v64, v92
	ds_write_b32 v142, v64
	v_cvt_pk_bf16_f32 v64, v65, v93
	ds_write_b32 v142, v64 offset:4
	v_cvt_pk_bf16_f32 v64, v66, v94
	ds_write_b32 v142, v64 offset:8
	v_cvt_pk_bf16_f32 v64, v67, v95
	ds_write_b32 v142, v64 offset:12
	s_waitcnt vmcnt(36)
	v_cvt_pk_bf16_f32 v64, v68, v96
	ds_write_b32 v142, v64 offset:1040
	v_cvt_pk_bf16_f32 v64, v69, v97
	ds_write_b32 v142, v64 offset:1044
	v_cvt_pk_bf16_f32 v64, v70, v98
	ds_write_b32 v142, v64 offset:1048
	v_cvt_pk_bf16_f32 v64, v71, v99
	ds_write_b32 v142, v64 offset:1052
	s_waitcnt vmcnt(34)
; __device__ __forceinline__ unsigned cvt_pk_bf16(float lo, float hi) { unsigned r; asm volatile("v_cvt_pk_bf16_f32 %0, %1, %2" : "=v"(r) : "v"(lo), "v"(hi)); return r; }
; #define GAS __attribute__((address_space(1)))
; #define LAS __attribute__((address_space(3)))
; #define LDS_WAIT() asm volatile("s_waitcnt lgkmcnt(0)" ::: "memory")
; __device__ __forceinline__ void conv_emit(const ConvSrc& c, int lane, LAS unsigned* P, const f32x4 (&ra)[8], const f32x4 (&rb)[8]) {
;     ...
;     for (int i = 0; i < 8; ++i) { const int kp2 = 4 * i + kq; LAS unsigned* d = P + kp2 * 65 + n4;
;         d[0] = pg8::cvt_pk_bf16(ra[i].x, rb[i].x); d[1] = pg8::cvt_pk_bf16(ra[i].y, rb[i].y); d[2] = pg8::cvt_pk_bf16(ra[i].z, rb[i].z); d[3] = pg8::cvt_pk_bf16(ra[i].w, rb[i].w); }
;     LDS_WAIT(); asm volatile("" ::: "memory");
;     const int cc = lane & 7;
; #pragma unroll
;     for (int jj = 0; jj < 8; ++jj) { const int n = (lane >> 3) + 8 * jj; const LAS unsigned* sp = P + (4 * cc) * 65 + n;
;         v4u o; o.x = sp[0]; o.y = sp[65]; o.z = sp[130]; o.w = sp[195];
;         bf16* dst = c.tiled ? c.WT + (size_t)((nb >> 2) * c.tiled + c.ktoff + kb) * 16384 + ((nb & 3) * 64 + n) * 64 + 8 * cc : c.WT + (size_t)(n0 + n) * c.ldk + k0 + 8 * cc;
;         __builtin_nontemporal_store(o, (GAS v4u*)dst); }
;     LDS_WAIT(); asm volatile("" ::: "memory");
	v_cvt_pk_bf16_f32 v64, v72, v100
	ds_write_b32 v142, v64 offset:2080
	v_cvt_pk_bf16_f32 v64, v73, v101
	ds_write_b32 v142, v64 offset:2084
	v_cvt_pk_bf16_f32 v64, v74, v102
	ds_write_b32 v142, v64 offset:2088
	v_cvt_pk_bf16_f32 v64, v75, v103
	ds_write_b32 v142, v64 offset:2092
	s_waitcnt vmcnt(32)
	v_cvt_pk_bf16_f32 v64, v76, v104
	ds_write_b32 v142, v64 offset:3120
	v_cvt_pk_bf16_f32 v64, v77, v105
	ds_write_b32 v142, v64 offset:3124
	v_cvt_pk_bf16_f32 v64, v78, v106
	ds_write_b32 v142, v64 offset:3128
	v_cvt_pk_bf16_f32 v64, v79, v107
	ds_write_b32 v142, v64 offset:3132
	s_waitcnt vmcnt(24)
	v_cvt_pk_bf16_f32 v64, v80, v108
	ds_write_b32 v142, v64 offset:4160
	v_cvt_pk_bf16_f32 v64, v81, v109
	ds_write_b32 v142, v64 offset:4164
	v_cvt_pk_bf16_f32 v64, v82, v110
	ds_write_b32 v142, v64 offset:4168
	v_cvt_pk_bf16_f32 v64, v83, v111
	ds_write_b32 v142, v64 offset:4172
	s_waitcnt vmcnt(28)
	v_cvt_pk_bf16_f32 v64, v84, v112
	ds_write_b32 v142, v64 offset:5200
	v_cvt_pk_bf16_f32 v64, v85, v113
	ds_write_b32 v142, v64 offset:5204
	v_cvt_pk_bf16_f32 v64, v86, v114
	ds_write_b32 v142, v64 offset:5208
	v_cvt_pk_bf16_f32 v64, v87, v115
	ds_write_b32 v142, v64 offset:5212
	s_waitcnt vmcnt(26)
	v_cvt_pk_bf16_f32 v64, v88, v116
	ds_write_b32 v142, v64 offset:6240
	v_cvt_pk_bf16_f32 v64, v89, v117
	ds_write_b32 v142, v64 offset:6244
	v_cvt_pk_bf16_f32 v64, v90, v118
	ds_write_b32 v142, v64 offset:6248
	v_cvt_pk_bf16_f32 v64, v91, v119
	ds_write_b32 v142, v64 offset:6252
	s_waitcnt vmcnt(24)
	v_cvt_pk_bf16_f32 v64, v120, v124
	ds_write_b32 v142, v64 offset:7280
	v_cvt_pk_bf16_f32 v64, v121, v125
	ds_write_b32 v142, v64 offset:7284
	v_cvt_pk_bf16_f32 v64, v122, v126
	ds_write_b32 v142, v64 offset:7288
	v_cvt_pk_bf16_f32 v64, v123, v127
	ds_write_b32 v142, v64 offset:7292
	s_ashr_i32 s4, s53, 2
	s_waitcnt lgkmcnt(0)
	s_mul_i32 s4, s4, s20
	s_add_i32 s5, s21, s5
	s_add_i32 s4, s5, s4
	ds_read2_b32 v[72:73], v134 offset1:8
	ds_read2_b32 v[64:65], v134 offset0:65 offset1:73
	ds_read2_b32 v[74:75], v134 offset0:130 offset1:138
	ds_read2_b32 v[66:67], v134 offset0:195 offset1:203
	s_ashr_i32 s5, s4, 31
	s_and_b32 s42, s42, 0xc0
	s_lshl_b64 s[4:5], s[4:5], 15
	s_add_u32 s40, s40, s4
	v_add_lshl_u32 v76, s42, v132, 6
	s_addc_u32 s41, s41, s5
	v_ashrrev_i32_e32 v77, 31, v76
	v_lshl_add_u64 v[76:77], v[76:77], 1, s[40:41]
	s_waitcnt lgkmcnt(3)
	v_mov_b32_e32 v68, v72
	s_waitcnt lgkmcnt(2)
	v_mov_b32_e32 v69, v64
	s_waitcnt lgkmcnt(1)
	v_mov_b32_e32 v70, v74
	s_waitcnt lgkmcnt(0)
	v_mov_b32_e32 v71, v66
	v_lshl_add_u64 v[76:77], v[76:77], 0, v[130:131]
	global_store_dwordx4 v[76:77], v[68:71], off nt
	v_mov_b32_e32 v64, v73
	v_mov_b32_e32 v66, v75
	v_add_lshl_u32 v68, s42, v135, 6
	v_ashrrev_i32_e32 v69, 31, v68
	v_lshl_add_u64 v[68:69], v[68:69], 1, s[40:41]
	v_lshl_add_u64 v[72:73], v[68:69], 0, v[130:131]
	ds_read2_b32 v[74:75], v134 offset0:16 offset1:24
	ds_read2_b32 v[68:69], v134 offset0:81 offset1:89
	ds_read2_b32 v[76:77], v134 offset0:146 offset1:154
	ds_read2_b32 v[70:71], v134 offset0:211 offset1:219
	global_store_dwordx4 v[72:73], v[64:67], off nt
	v_add_lshl_u32 v72, s42, v136, 6
	v_ashrrev_i32_e32 v73, 31, v72
	v_lshl_add_u64 v[72:73], v[72:73], 1, s[40:41]
	s_waitcnt lgkmcnt(3)
	v_mov_b32_e32 v64, v74
	s_waitcnt lgkmcnt(2)
	v_mov_b32_e32 v65, v68
	s_waitcnt lgkmcnt(1)
	v_mov_b32_e32 v66, v76
	s_waitcnt lgkmcnt(0)
	v_mov_b32_e32 v67, v70
	v_lshl_add_u64 v[72:73], v[72:73], 0, v[130:131]
	global_store_dwordx4 v[72:73], v[64:67], off nt
	v_mov_b32_e32 v68, v75
	v_mov_b32_e32 v70, v77
	v_add_lshl_u32 v64, s42, v137, 6
	v_ashrrev_i32_e32 v65, 31, v64
	v_lshl_add_u64 v[64:65], v[64:65], 1, s[40:41]
	v_lshl_add_u64 v[72:73], v[64:65], 0, v[130:131]
	ds_read2_b32 v[74:75], v134 offset0:32 offset1:40
	ds_read2_b32 v[64:65], v134 offset0:97 offset1:105
	ds_read2_b32 v[76:77], v134 offset0:162 offset1:170
	ds_read2_b32 v[66:67], v134 offset0:227 offset1:235
	global_store_dwordx4 v[72:73], v[68:71], off nt
	v_add_lshl_u32 v72, s42, v138, 6
	v_ashrrev_i32_e32 v73, 31, v72
	v_lshl_add_u64 v[72:73], v[72:73], 1, s[40:41]
	s_waitcnt lgkmcnt(3)
	v_mov_b32_e32 v68, v74
	s_waitcnt lgkmcnt(2)
	v_mov_b32_e32 v69, v64
	s_waitcnt lgkmcnt(1)
	v_mov_b32_e32 v70, v76
	s_waitcnt lgkmcnt(0)
	v_mov_b32_e32 v71, v66
	v_lshl_add_u64 v[72:73], v[72:73], 0, v[130:131]
	global_store_dwordx4 v[72:73], v[68:71], off nt
	v_mov_b32_e32 v64, v75
	v_mov_b32_e32 v66, v77
	v_add_lshl_u32 v68, s42, v139, 6
	v_ashrrev_i32_e32 v69, 31, v68
	v_lshl_add_u64 v[68:69], v[68:69], 1, s[40:41]
	v_lshl_add_u64 v[72:73], v[68:69], 0, v[130:131]
	ds_read2_b32 v[74:75], v134 offset0:48 offset1:56
	ds_read2_b32 v[68:69], v134 offset0:113 offset1:121
	ds_read2_b32 v[76:77], v134 offset0:178 offset1:186
	ds_read2_b32 v[70:71], v134 offset0:243 offset1:251
	global_store_dwordx4 v[72:73], v[64:67], off nt
	v_add_lshl_u32 v72, s42, v140, 6
	v_ashrrev_i32_e32 v73, 31, v72
	v_lshl_add_u64 v[72:73], v[72:73], 1, s[40:41]
	s_waitcnt lgkmcnt(3)
	v_mov_b32_e32 v64, v74
	s_waitcnt lgkmcnt(2)
	v_mov_b32_e32 v65, v68
	s_waitcnt lgkmcnt(1)
	v_mov_b32_e32 v66, v76
	s_waitcnt lgkmcnt(0)
	v_mov_b32_e32 v67, v70
	v_lshl_add_u64 v[72:73], v[72:73], 0, v[130:131]
	global_store_dwordx4 v[72:73], v[64:67], off nt
	v_mov_b32_e32 v68, v75
	v_mov_b32_e32 v70, v77
	v_add_lshl_u32 v64, s42, v141, 6
	v_ashrrev_i32_e32 v65, 31, v64
	v_lshl_add_u64 v[64:65], v[64:65], 1, s[40:41]
	v_lshl_add_u64 v[64:65], v[64:65], 0, v[130:131]
	global_store_dwordx4 v[64:65], v[68:71], off nt
	s_waitcnt lgkmcnt(0)
	s_cmp_lt_i32 s22, s17
	s_mov_b32 s4, s28
	s_cbranch_scc0 .LBB0_2288

; #define GAS __attribute__((address_space(1)))
; __device__ __forceinline__ float dot4(f32x4 a, f32x4 b) { return (a.x * b.x + a.y * b.y) + (a.z * b.z + a.w * b.w); }
; __device__ __forceinline__ f32x4 unpack4(u32x2 w) { return (f32x4){bflo(w.x), bfhi(w.x), bflo(w.y), bfhi(w.y)}; }
; __device__ __forceinline__ void phase12(KP kp, LAS unsigned char* lds, int wave, int bid, int G) {
;     ...
;     for (int m = bid * NWAVES + wave; m < T; m += G * NWAVES) {
;         const GAS f32x4* xr = (const GAS f32x4*)(X1 + (size_t)m * DM) + lane;
;         const i32x4 te = *(const GAS i32x4*)(TOPI + m * 4), rk = *(const GAS i32x4*)(TRANK + m * 4); const f32x4 tw = *(const GAS f32x4*)(TOPW + m * 4);
;         const i32x4 sl = (i32x4){pstart[te.x] + rk.x, pstart[te.y] + rk.y, pstart[te.z] + rk.z, pstart[te.w] + rk.w};
;         const GAS u32x2* y0 = (const GAS u32x2*)(YS + (size_t)sl.x * DM) + lane; const GAS u32x2* y1 = (const GAS u32x2*)(YS + (size_t)sl.y * DM) + lane;
;         const GAS u32x2* y2 = (const GAS u32x2*)(YS + (size_t)sl.z * DM) + lane; const GAS u32x2* y3 = (const GAS u32x2*)(YS + (size_t)sl.w * DM) + lane;
;         f32x4 v[8]; float s = 0.f;
; #pragma unroll
;         for (int j = 0; j < 8; ++j) {
;             const f32x4 mo = tw.x * unpack4(y0[64 * j]) + tw.y * unpack4(y1[64 * j]) + tw.z * unpack4(y2[64 * j]) + tw.w * unpack4(y3[64 * j]);
;             const f32x4 g2 = *(const GAS f32x4*)(mod + 5 * 2048 + 256 * j + 4 * lane);
;             v[j] = xr[64 * j] + g2 * mo; s += dot4(v[j], v[j]); }
.LBB0_4682:
	v_lshl_add_u64 v[36:37], s[12:13], 0, v[90:91]
	s_ashr_i32 s5, s4, 31
	v_add_co_u32_e32 v104, vcc, s7, v36
	s_lshl_b64 s[0:1], s[4:5], 2
	s_nop 0
	v_addc_co_u32_e32 v105, vcc, 0, v37, vcc
	v_add_co_u32_e32 v106, vcc, s21, v36
	s_add_u32 s24, s14, s0
	s_nop 0
	v_addc_co_u32_e32 v107, vcc, 0, v37, vcc
	s_addc_u32 s25, s15, s1
	global_load_dwordx4 v[0:3], v[70:71], off
	global_load_dwordx4 v[4:7], v[70:71], off offset:1024
	global_load_dwordx4 v[8:11], v[70:71], off offset:2048
	global_load_dwordx4 v[12:15], v[70:71], off offset:3072
	global_load_dwordx4 v[16:19], v[74:75], off
	global_load_dwordx4 v[20:23], v[76:77], off
	global_load_dwordx4 v[24:27], v[78:79], off
	global_load_dwordx4 v[32:35], v[80:81], off
	global_load_dwordx4 v[28:31], v[72:73], off
	global_load_dwordx4 v[60:63], v[104:105], off offset:1024
	global_load_dwordx4 v[56:59], v[104:105], off offset:2048
	global_load_dwordx4 v[48:51], v[104:105], off offset:3072
	global_load_dwordx4 v[64:67], v[106:107], off offset:-4096
	global_load_dwordx4 v[52:55], v[106:107], off
	global_load_dwordx4 v[44:47], v[106:107], off offset:1024
	global_load_dwordx4 v[40:43], v[106:107], off offset:2048
	global_load_dwordx4 v[36:39], v[106:107], off offset:3072
	v_lshl_add_u64 v[92:93], s[8:9], 0, v[90:91]
	global_load_dwordx4 v[104:107], v100, s[24:25]
	s_add_u32 s24, s17, s0
	s_addc_u32 s25, s18, s1
	global_load_dwordx4 v[108:111], v100, s[24:25]
	s_add_u32 s0, s19, s0
	s_addc_u32 s1, s20, s1
	global_load_dwordx4 v[112:115], v100, s[0:1]
	s_add_i32 s2, s2, s6
	s_add_i32 s4, s4, s16
	s_add_u32 s8, s8, s10
	s_addc_u32 s9, s9, s11
	s_add_u32 s12, s12, s10
	s_addc_u32 s13, s13, s11
	s_cmpk_lt_i32 s2, 0x2000
	s_waitcnt vmcnt(2)
	v_lshlrev_b32_e32 v103, 2, v104
	v_lshlrev_b32_e32 v104, 2, v105
	v_lshlrev_b32_e32 v105, 2, v106
	v_lshlrev_b32_e32 v106, 2, v107
	v_add_u32_e32 v103, s3, v103
	v_add_u32_e32 v105, s3, v105
	v_add_u32_e32 v104, s3, v104
	v_add_u32_e32 v106, s3, v106
	ds_read_b32 v103, v103
	ds_read_b32 v107, v104
	ds_read_b32 v105, v105
	ds_read_b32 v116, v106
	s_waitcnt vmcnt(0)
	v_mov_b32_e32 v104, v115
	s_waitcnt lgkmcnt(3)
	v_add_u32_e32 v106, v103, v108
	s_waitcnt lgkmcnt(2)
	v_add_u32_e32 v108, v107, v109
	s_waitcnt lgkmcnt(1)
	v_add_u32_e32 v110, v105, v110
	s_waitcnt lgkmcnt(0)
	v_add_u32_e32 v116, v116, v111
	v_ashrrev_i32_e32 v107, 31, v106
	v_ashrrev_i32_e32 v109, 31, v108
	v_ashrrev_i32_e32 v111, 31, v110
	v_ashrrev_i32_e32 v117, 31, v116
	v_lshlrev_b64 v[106:107], 12, v[106:107]
	v_lshlrev_b64 v[108:109], 12, v[108:109]
	v_lshlrev_b64 v[110:111], 12, v[110:111]
	v_lshlrev_b64 v[116:117], 12, v[116:117]
	v_lshl_add_u64 v[106:107], v[68:69], 0, v[106:107]
	v_lshl_add_u64 v[108:109], v[68:69], 0, v[108:109]
	v_lshl_add_u64 v[110:111], v[68:69], 0, v[110:111]
	v_lshl_add_u64 v[116:117], v[68:69], 0, v[116:117]
	global_load_dwordx2 v[118:119], v[106:107], off
	global_load_dwordx2 v[120:121], v[108:109], off
	global_load_dwordx2 v[122:123], v[110:111], off
	global_load_dwordx2 v[124:125], v[116:117], off
	global_load_dwordx2 v[126:127], v[106:107], off offset:512
	global_load_dwordx2 v[128:129], v[108:109], off offset:512
	global_load_dwordx2 v[130:131], v[110:111], off offset:512
	global_load_dwordx2 v[132:133], v[116:117], off offset:512
	global_load_dwordx2 v[134:135], v[106:107], off offset:1024
	global_load_dwordx2 v[136:137], v[108:109], off offset:1024
	global_load_dwordx2 v[138:139], v[110:111], off offset:1024
	global_load_dwordx2 v[140:141], v[116:117], off offset:1024
	global_load_dwordx2 v[142:143], v[106:107], off offset:1536
	global_load_dwordx2 v[144:145], v[108:109], off offset:1536
	global_load_dwordx2 v[146:147], v[110:111], off offset:1536
	global_load_dwordx2 v[148:149], v[116:117], off offset:1536
	global_load_dwordx2 v[150:151], v[106:107], off offset:2048
	global_load_dwordx2 v[152:153], v[106:107], off offset:2560
	global_load_dwordx2 v[154:155], v[106:107], off offset:3072
	s_nop 0
	global_load_dwordx2 v[106:107], v[106:107], off offset:3584
	s_nop 0
	global_load_dwordx2 v[156:157], v[108:109], off offset:2048
	global_load_dwordx2 v[158:159], v[108:109], off offset:2560
	global_load_dwordx2 v[160:161], v[108:109], off offset:3072
	s_nop 0
	global_load_dwordx2 v[108:109], v[108:109], off offset:3584
	s_nop 0
	global_load_dwordx2 v[162:163], v[110:111], off offset:2048
	global_load_dwordx2 v[164:165], v[110:111], off offset:2560
	global_load_dwordx2 v[166:167], v[110:111], off offset:3072
	s_nop 0
	global_load_dwordx2 v[110:111], v[110:111], off offset:3584
	s_nop 0
	global_load_dwordx2 v[168:169], v[116:117], off offset:2048
	global_load_dwordx2 v[170:171], v[116:117], off offset:2560
	global_load_dwordx2 v[172:173], v[116:117], off offset:3072
	s_nop 0
	global_load_dwordx2 v[116:117], v[116:117], off offset:3584
	s_waitcnt vmcnt(31)
	v_lshlrev_b32_e32 v174, 16, v118
	s_waitcnt vmcnt(24)
	v_lshlrev_b32_e32 v176, 16, v120
	v_and_b32_e32 v177, 0xffff0000, v120
	v_lshlrev_b32_e32 v120, 16, v121
	v_and_b32_e32 v121, 0xffff0000, v121
	s_waitcnt vmcnt(26)
	v_lshlrev_b32_e32 v184, 16, v128
	v_and_b32_e32 v185, 0xffff0000, v128
	v_lshlrev_b32_e32 v128, 16, v129
	v_and_b32_e32 v129, 0xffff0000, v129
	v_and_b32_e32 v175, 0xffff0000, v118
	v_lshlrev_b32_e32 v118, 16, v119
	v_and_b32_e32 v119, 0xffff0000, v119
	v_lshlrev_b32_e32 v182, 16, v126
	v_and_b32_e32 v183, 0xffff0000, v126
	v_lshlrev_b32_e32 v126, 16, v127
	v_and_b32_e32 v127, 0xffff0000, v127
	s_waitcnt vmcnt(22)
	v_lshlrev_b32_e32 v192, 16, v136
	v_and_b32_e32 v193, 0xffff0000, v136
	v_lshlrev_b32_e32 v136, 16, v137
	v_and_b32_e32 v137, 0xffff0000, v137
	s_waitcnt vmcnt(18)
; __device__ __forceinline__ f32x4 unpack4(u32x2 w) { return (f32x4){bflo(w.x), bfhi(w.x), bflo(w.y), bfhi(w.y)}; }
; __device__ __forceinline__ void phase12(KP kp, LAS unsigned char* lds, int wave, int bid, int G) {
;     ...
;         for (int j = 0; j < 8; ++j) {
;             const f32x4 mo = tw.x * unpack4(y0[64 * j]) + tw.y * unpack4(y1[64 * j]) + tw.z * unpack4(y2[64 * j]) + tw.w * unpack4(y3[64 * j]);
	v_lshlrev_b32_e32 v200, 16, v144
	v_and_b32_e32 v201, 0xffff0000, v144
	v_lshlrev_b32_e32 v144, 16, v145
	v_and_b32_e32 v145, 0xffff0000, v145
	s_waitcnt vmcnt(11)
	v_lshlrev_b32_e32 v208, 16, v156
	v_and_b32_e32 v209, 0xffff0000, v156
	v_lshlrev_b32_e32 v156, 16, v157
	v_and_b32_e32 v157, 0xffff0000, v157
	s_waitcnt vmcnt(10)
	v_lshlrev_b32_e32 v216, 16, v158
	v_and_b32_e32 v217, 0xffff0000, v158
	v_lshlrev_b32_e32 v158, 16, v159
	v_and_b32_e32 v159, 0xffff0000, v159
	s_waitcnt vmcnt(9)
	v_lshlrev_b32_e32 v224, 16, v160
	v_and_b32_e32 v225, 0xffff0000, v160
	v_lshlrev_b32_e32 v160, 16, v161
	v_and_b32_e32 v161, 0xffff0000, v161
	s_waitcnt vmcnt(8)
	v_lshlrev_b32_e32 v232, 16, v108
	v_and_b32_e32 v233, 0xffff0000, v108
	v_lshlrev_b32_e32 v108, 16, v109
	v_and_b32_e32 v109, 0xffff0000, v109
	v_pk_mul_f32 v[120:121], v[112:113], v[120:121] op_sel:[1,0]
	v_pk_mul_f32 v[176:177], v[112:113], v[176:177] op_sel:[1,0]
	v_pk_mul_f32 v[128:129], v[112:113], v[128:129] op_sel:[1,0]
	v_pk_mul_f32 v[184:185], v[112:113], v[184:185] op_sel:[1,0]
	v_lshlrev_b32_e32 v178, 16, v122
	v_and_b32_e32 v179, 0xffff0000, v122
	v_lshlrev_b32_e32 v122, 16, v123
	v_and_b32_e32 v123, 0xffff0000, v123
	v_lshlrev_b32_e32 v186, 16, v130
	v_and_b32_e32 v187, 0xffff0000, v130
	v_lshlrev_b32_e32 v130, 16, v131
	v_and_b32_e32 v131, 0xffff0000, v131
	v_lshlrev_b32_e32 v190, 16, v134
	v_and_b32_e32 v191, 0xffff0000, v134
	v_lshlrev_b32_e32 v134, 16, v135
	v_and_b32_e32 v135, 0xffff0000, v135
	v_lshlrev_b32_e32 v198, 16, v142
	v_and_b32_e32 v199, 0xffff0000, v142
	v_lshlrev_b32_e32 v142, 16, v143
	v_and_b32_e32 v143, 0xffff0000, v143
	v_lshlrev_b32_e32 v206, 16, v150
	v_and_b32_e32 v207, 0xffff0000, v150
	v_lshlrev_b32_e32 v150, 16, v151
	v_and_b32_e32 v151, 0xffff0000, v151
	v_lshlrev_b32_e32 v214, 16, v152
	v_and_b32_e32 v215, 0xffff0000, v152
	v_lshlrev_b32_e32 v152, 16, v153
	v_and_b32_e32 v153, 0xffff0000, v153
	v_lshlrev_b32_e32 v222, 16, v154
	v_and_b32_e32 v223, 0xffff0000, v154
	v_lshlrev_b32_e32 v154, 16, v155
	v_and_b32_e32 v155, 0xffff0000, v155
	v_lshlrev_b32_e32 v230, 16, v106
	v_and_b32_e32 v231, 0xffff0000, v106
	v_lshlrev_b32_e32 v106, 16, v107
	v_and_b32_e32 v107, 0xffff0000, v107
	v_pk_mul_f32 v[192:193], v[112:113], v[192:193] op_sel:[1,0]
	v_pk_mul_f32 v[136:137], v[112:113], v[136:137] op_sel:[1,0]
	v_pk_mul_f32 v[144:145], v[112:113], v[144:145] op_sel:[1,0]
	v_pk_mul_f32 v[200:201], v[112:113], v[200:201] op_sel:[1,0]
	v_pk_mul_f32 v[156:157], v[112:113], v[156:157] op_sel:[1,0]
	v_pk_mul_f32 v[208:209], v[112:113], v[208:209] op_sel:[1,0]
	v_pk_mul_f32 v[216:217], v[112:113], v[216:217] op_sel:[1,0]
	v_pk_mul_f32 v[158:159], v[112:113], v[158:159] op_sel:[1,0]
	v_pk_mul_f32 v[160:161], v[112:113], v[160:161] op_sel:[1,0]
	v_pk_mul_f32 v[224:225], v[112:113], v[224:225] op_sel:[1,0]
	v_pk_mul_f32 v[108:109], v[112:113], v[108:109] op_sel:[1,0]
	v_pk_mul_f32 v[232:233], v[112:113], v[232:233] op_sel:[1,0]
	v_pk_fma_f32 v[174:175], v[112:113], v[174:175], v[176:177] op_sel_hi:[0,1,1]
	v_pk_fma_f32 v[118:119], v[112:113], v[118:119], v[120:121] op_sel_hi:[0,1,1]
	v_pk_fma_f32 v[120:121], v[112:113], v[182:183], v[184:185] op_sel_hi:[0,1,1]
	v_pk_fma_f32 v[126:127], v[112:113], v[126:127], v[128:129] op_sel_hi:[0,1,1]
	v_lshlrev_b32_e32 v180, 16, v124
	v_and_b32_e32 v181, 0xffff0000, v124
	v_lshlrev_b32_e32 v124, 16, v125
	v_and_b32_e32 v125, 0xffff0000, v125
	v_lshlrev_b32_e32 v188, 16, v132
	v_and_b32_e32 v189, 0xffff0000, v132
	v_lshlrev_b32_e32 v132, 16, v133
	v_and_b32_e32 v133, 0xffff0000, v133
	v_lshlrev_b32_e32 v194, 16, v138
	v_and_b32_e32 v195, 0xffff0000, v138
	v_lshlrev_b32_e32 v138, 16, v139
	v_and_b32_e32 v139, 0xffff0000, v139
	v_lshlrev_b32_e32 v202, 16, v146
	v_and_b32_e32 v203, 0xffff0000, v146
	v_lshlrev_b32_e32 v146, 16, v147
	v_and_b32_e32 v147, 0xffff0000, v147
	s_waitcnt vmcnt(7)
	v_lshlrev_b32_e32 v210, 16, v162
	v_and_b32_e32 v211, 0xffff0000, v162
	v_lshlrev_b32_e32 v162, 16, v163
	v_and_b32_e32 v163, 0xffff0000, v163
	s_waitcnt vmcnt(6)
	v_lshlrev_b32_e32 v218, 16, v164
	v_and_b32_e32 v219, 0xffff0000, v164
	v_lshlrev_b32_e32 v164, 16, v165
	v_and_b32_e32 v165, 0xffff0000, v165
	s_waitcnt vmcnt(5)
	v_lshlrev_b32_e32 v226, 16, v166
	v_and_b32_e32 v227, 0xffff0000, v166
	v_lshlrev_b32_e32 v166, 16, v167
	v_and_b32_e32 v167, 0xffff0000, v167
	s_waitcnt vmcnt(4)
	v_lshlrev_b32_e32 v234, 16, v110
	v_and_b32_e32 v235, 0xffff0000, v110
	v_lshlrev_b32_e32 v110, 16, v111
	v_and_b32_e32 v111, 0xffff0000, v111
	v_pk_fma_f32 v[128:129], v[112:113], v[134:135], v[136:137] op_sel_hi:[0,1,1]
	v_pk_fma_f32 v[134:135], v[112:113], v[190:191], v[192:193] op_sel_hi:[0,1,1]
	v_pk_fma_f32 v[136:137], v[112:113], v[198:199], v[200:201] op_sel_hi:[0,1,1]
	v_pk_fma_f32 v[142:143], v[112:113], v[142:143], v[144:145] op_sel_hi:[0,1,1]
	v_pk_fma_f32 v[144:145], v[112:113], v[206:207], v[208:209] op_sel_hi:[0,1,1]
	v_pk_fma_f32 v[150:151], v[112:113], v[150:151], v[156:157] op_sel_hi:[0,1,1]
	v_pk_fma_f32 v[152:153], v[112:113], v[152:153], v[158:159] op_sel_hi:[0,1,1]
	v_pk_fma_f32 v[156:157], v[112:113], v[214:215], v[216:217] op_sel_hi:[0,1,1]
	v_pk_fma_f32 v[158:159], v[112:113], v[222:223], v[224:225] op_sel_hi:[0,1,1]
	v_pk_fma_f32 v[154:155], v[112:113], v[154:155], v[160:161] op_sel_hi:[0,1,1]
	v_pk_fma_f32 v[160:161], v[112:113], v[230:231], v[232:233] op_sel_hi:[0,1,1]
	v_pk_fma_f32 v[106:107], v[112:113], v[106:107], v[108:109] op_sel_hi:[0,1,1]
	v_pk_fma_f32 v[108:109], v[114:115], v[122:123], v[118:119] op_sel_hi:[0,1,1]
	v_pk_fma_f32 v[112:113], v[114:115], v[178:179], v[174:175] op_sel_hi:[0,1,1]
	v_pk_fma_f32 v[118:119], v[114:115], v[130:131], v[126:127] op_sel_hi:[0,1,1]
	v_pk_fma_f32 v[120:121], v[114:115], v[186:187], v[120:121] op_sel_hi:[0,1,1]
	v_lshlrev_b32_e32 v196, 16, v140
	v_and_b32_e32 v197, 0xffff0000, v140
	v_lshlrev_b32_e32 v140, 16, v141
	v_and_b32_e32 v141, 0xffff0000, v141
	v_lshlrev_b32_e32 v204, 16, v148
	v_and_b32_e32 v205, 0xffff0000, v148
	v_lshlrev_b32_e32 v148, 16, v149
	v_and_b32_e32 v149, 0xffff0000, v149
	s_waitcnt vmcnt(3)
; #define GAS __attribute__((address_space(1)))
; __device__ __forceinline__ float dot4(f32x4 a, f32x4 b) { return (a.x * b.x + a.y * b.y) + (a.z * b.z + a.w * b.w); }
; __device__ __forceinline__ f32x4 unpack4(u32x2 w) { return (f32x4){bflo(w.x), bfhi(w.x), bflo(w.y), bfhi(w.y)}; }
; __device__ __forceinline__ void phase12(KP kp, LAS unsigned char* lds, int wave, int bid, int G) {
;     ...
;             const f32x4 mo = tw.x * unpack4(y0[64 * j]) + tw.y * unpack4(y1[64 * j]) + tw.z * unpack4(y2[64 * j]) + tw.w * unpack4(y3[64 * j]);
;             const f32x4 g2 = *(const GAS f32x4*)(mod + 5 * 2048 + 256 * j + 4 * lane);
;             v[j] = xr[64 * j] + g2 * mo; s += dot4(v[j], v[j]); }
;         const float rstd = 1.0f / sqrtf(wave_sum(s) * (1.0f / DM) + EPS);
	v_lshlrev_b32_e32 v212, 16, v168
	v_and_b32_e32 v213, 0xffff0000, v168
	v_lshlrev_b32_e32 v168, 16, v169
	v_and_b32_e32 v169, 0xffff0000, v169
	s_waitcnt vmcnt(2)
	v_lshlrev_b32_e32 v220, 16, v170
	v_and_b32_e32 v221, 0xffff0000, v170
	v_lshlrev_b32_e32 v170, 16, v171
	v_and_b32_e32 v171, 0xffff0000, v171
	s_waitcnt vmcnt(1)
	v_lshlrev_b32_e32 v228, 16, v172
	v_and_b32_e32 v229, 0xffff0000, v172
	v_lshlrev_b32_e32 v172, 16, v173
	v_and_b32_e32 v173, 0xffff0000, v173
	s_waitcnt vmcnt(0)
	v_lshlrev_b32_e32 v236, 16, v116
	v_and_b32_e32 v237, 0xffff0000, v116
	v_lshlrev_b32_e32 v116, 16, v117
	v_and_b32_e32 v117, 0xffff0000, v117
	v_pk_fma_f32 v[122:123], v[114:115], v[194:195], v[134:135] op_sel_hi:[0,1,1]
	v_pk_fma_f32 v[126:127], v[114:115], v[138:139], v[128:129] op_sel_hi:[0,1,1]
	v_pk_fma_f32 v[128:129], v[114:115], v[146:147], v[142:143] op_sel_hi:[0,1,1]
	v_pk_fma_f32 v[130:131], v[114:115], v[202:203], v[136:137] op_sel_hi:[0,1,1]
	v_pk_fma_f32 v[134:135], v[114:115], v[162:163], v[150:151] op_sel_hi:[0,1,1]
	v_pk_fma_f32 v[136:137], v[114:115], v[210:211], v[144:145] op_sel_hi:[0,1,1]
	v_pk_fma_f32 v[138:139], v[114:115], v[218:219], v[156:157] op_sel_hi:[0,1,1]
	v_pk_fma_f32 v[142:143], v[114:115], v[164:165], v[152:153] op_sel_hi:[0,1,1]
	v_pk_fma_f32 v[144:145], v[114:115], v[166:167], v[154:155] op_sel_hi:[0,1,1]
	v_pk_fma_f32 v[146:147], v[114:115], v[226:227], v[158:159] op_sel_hi:[0,1,1]
	v_pk_fma_f32 v[106:107], v[114:115], v[110:111], v[106:107] op_sel_hi:[0,1,1]
	v_pk_fma_f32 v[110:111], v[114:115], v[234:235], v[160:161] op_sel_hi:[0,1,1]
	v_pk_fma_f32 v[112:113], v[104:105], v[180:181], v[112:113] op_sel_hi:[0,1,1]
	v_pk_fma_f32 v[108:109], v[104:105], v[124:125], v[108:109] op_sel_hi:[0,1,1]
	v_pk_fma_f32 v[114:115], v[104:105], v[188:189], v[120:121] op_sel_hi:[0,1,1]
	v_pk_fma_f32 v[118:119], v[104:105], v[132:133], v[118:119] op_sel_hi:[0,1,1]
	v_pk_fma_f32 v[120:121], v[104:105], v[140:141], v[126:127] op_sel_hi:[0,1,1]
	v_pk_fma_f32 v[122:123], v[104:105], v[196:197], v[122:123] op_sel_hi:[0,1,1]
	v_pk_fma_f32 v[124:125], v[104:105], v[204:205], v[130:131] op_sel_hi:[0,1,1]
	v_pk_fma_f32 v[126:127], v[104:105], v[148:149], v[128:129] op_sel_hi:[0,1,1]
	v_pk_fma_f32 v[128:129], v[104:105], v[212:213], v[136:137] op_sel_hi:[0,1,1]
	v_pk_fma_f32 v[130:131], v[104:105], v[168:169], v[134:135] op_sel_hi:[0,1,1]
	v_pk_fma_f32 v[132:133], v[104:105], v[170:171], v[142:143] op_sel_hi:[0,1,1]
	v_pk_fma_f32 v[134:135], v[104:105], v[220:221], v[138:139] op_sel_hi:[0,1,1]
	v_pk_fma_f32 v[136:137], v[104:105], v[228:229], v[146:147] op_sel_hi:[0,1,1]
	v_pk_fma_f32 v[138:139], v[104:105], v[172:173], v[144:145] op_sel_hi:[0,1,1]
	v_pk_fma_f32 v[110:111], v[104:105], v[236:237], v[110:111] op_sel_hi:[0,1,1]
	v_pk_fma_f32 v[104:105], v[104:105], v[116:117], v[106:107] op_sel_hi:[0,1,1]
	v_pk_fma_f32 v[2:3], v[2:3], v[108:109], v[66:67]
	v_pk_fma_f32 v[0:1], v[0:1], v[112:113], v[64:65]
	v_pk_fma_f32 v[6:7], v[6:7], v[118:119], v[62:63]
	v_pk_fma_f32 v[4:5], v[4:5], v[114:115], v[60:61]
	v_pk_fma_f32 v[8:9], v[8:9], v[122:123], v[56:57]
	v_pk_fma_f32 v[10:11], v[10:11], v[120:121], v[58:59]
	v_pk_fma_f32 v[26:27], v[26:27], v[138:139], v[42:43]
	v_pk_fma_f32 v[34:35], v[34:35], v[104:105], v[38:39]
	v_mov_b32_e32 v38, v1
	v_mov_b32_e32 v39, v5
	v_mov_b32_e32 v42, v3
	v_mov_b32_e32 v43, v7
	v_pk_fma_f32 v[20:21], v[20:21], v[134:135], v[44:45]
	v_pk_fma_f32 v[22:23], v[22:23], v[132:133], v[46:47]
	v_pk_fma_f32 v[24:25], v[24:25], v[136:137], v[40:41]
	v_pk_fma_f32 v[32:33], v[32:33], v[110:111], v[36:37]
	v_mov_b32_e32 v36, v0
	v_mov_b32_e32 v37, v4
	v_mov_b32_e32 v40, v2
	v_mov_b32_e32 v41, v6
	v_pk_mul_f32 v[44:45], v[10:11], v[10:11]
	v_pk_mul_f32 v[46:47], v[8:9], v[8:9]
	v_pk_mul_f32 v[38:39], v[38:39], v[38:39]
	v_pk_mul_f32 v[42:43], v[42:43], v[42:43]
	v_pk_fma_f32 v[14:15], v[14:15], v[126:127], v[50:51]
	v_pk_fma_f32 v[12:13], v[12:13], v[124:125], v[48:49]
	v_pk_mov_b32 v[60:61], v[46:47], v[44:45] op_sel:[1,0]
	v_mov_b32_e32 v47, v45
	v_pk_fma_f32 v[36:37], v[36:37], v[36:37], v[38:39]
	v_pk_fma_f32 v[38:39], v[40:41], v[40:41], v[42:43]
	v_pk_fma_f32 v[18:19], v[18:19], v[130:131], v[54:55]
	v_pk_fma_f32 v[16:17], v[16:17], v[128:129], v[52:53]
	v_mul_f32_e32 v48, v13, v13
	v_mul_f32_e32 v50, v15, v15
	v_pk_add_f32 v[40:41], v[60:61], v[46:47]
	v_pk_add_f32 v[36:37], v[36:37], v[38:39]
	v_mul_f32_e32 v59, v16, v16
	v_mul_f32_e32 v62, v17, v17
	v_mul_f32_e32 v63, v18, v18
	v_mul_f32_e32 v64, v19, v19
	v_pk_fma_f32 v[44:45], v[12:13], v[12:13], v[48:49] op_sel_hi:[1,1,0]
	v_pk_fma_f32 v[48:49], v[14:15], v[14:15], v[50:51] op_sel_hi:[1,1,0]
	v_pk_add_f32 v[38:39], v[40:41], v[40:41] op_sel:[0,1] op_sel_hi:[1,0]
	v_pk_add_f32 v[36:37], v[36:37], v[36:37] op_sel:[0,1] op_sel_hi:[1,0]
	v_pk_mul_f32 v[52:53], v[22:23], v[22:23]
	v_pk_mul_f32 v[54:55], v[20:21], v[20:21]
	v_mov_b32_e32 v45, v63
	v_mov_b32_e32 v49, v64
	v_mov_b32_e32 v39, v62
	v_mov_b32_e32 v37, v59
; #define GAS __attribute__((address_space(1)))
; __device__ __forceinline__ float dot4(f32x4 a, f32x4 b) { return (a.x * b.x + a.y * b.y) + (a.z * b.z + a.w * b.w); }
; __device__ __forceinline__ void phase12(KP kp, LAS unsigned char* lds, int wave, int bid, int G) {
;     ...
;             v[j] = xr[64 * j] + g2 * mo; s += dot4(v[j], v[j]); }
;         const float rstd = 1.0f / sqrtf(wave_sum(s) * (1.0f / DM) + EPS);
;         GAS f32x4* o = (GAS f32x4*)(KOUT() + (size_t)m * DM) + lane;
; #pragma unroll
;         for (int j = 0; j < 8; ++j) o[64 * j] = v[j] * rstd * *(const GAS f32x4*)(fg + 256 * j + 4 * lane);
;     }
	v_pk_mov_b32 v[50:51], v[54:55], v[52:53] op_sel:[1,0]
	v_mov_b32_e32 v55, v53
	v_pk_add_f32 v[40:41], v[44:45], v[48:49]
	v_pk_add_f32 v[36:37], v[36:37], v[38:39]
	v_mul_f32_e32 v56, v25, v25
	v_mul_f32_e32 v58, v27, v27
	v_pk_add_f32 v[42:43], v[50:51], v[54:55]
	v_pk_add_f32 v[36:37], v[36:37], v[40:41]
	v_mul_f32_e32 v65, v32, v32
	v_mul_f32_e32 v66, v33, v33
	v_mul_f32_e32 v67, v34, v34
	v_mul_f32_e32 v103, v35, v35
	v_pk_fma_f32 v[52:53], v[24:25], v[24:25], v[56:57] op_sel_hi:[1,1,0]
	v_pk_fma_f32 v[56:57], v[26:27], v[26:27], v[58:59] op_sel_hi:[1,1,0]
	v_pk_add_f32 v[42:43], v[42:43], v[42:43] op_sel:[0,1] op_sel_hi:[1,0]
	v_pk_add_f32 v[36:37], v[36:37], v[36:37] op_sel:[0,1] op_sel_hi:[1,0]
	v_mov_b32_e32 v53, v67
	v_mov_b32_e32 v57, v103
	v_mov_b32_e32 v43, v66
	v_mov_b32_e32 v37, v65
	v_pk_add_f32 v[44:45], v[52:53], v[56:57]
	v_pk_add_f32 v[36:37], v[36:37], v[42:43]
	s_nop 0
	v_pk_add_f32 v[36:37], v[36:37], v[44:45]
	s_nop 0
	v_add_f32_e32 v36, v36, v37
	s_nop 1
	v_add_f32_dpp v36, v36, v36 quad_perm:[1,0,3,2] row_mask:0xf bank_mask:0xf
	s_nop 1
	v_add_f32_dpp v36, v36, v36 quad_perm:[2,3,0,1] row_mask:0xf bank_mask:0xf
	s_nop 1
	v_add_f32_dpp v36, v36, v36 row_half_mirror row_mask:0xf bank_mask:0xf
	s_nop 1
	v_add_f32_dpp v36, v36, v36 row_mirror row_mask:0xf bank_mask:0xf
	v_mov_b32_e32 v37, v36
	s_nop 1
	v_permlane16_swap_b32_e32 v36, v37
	v_add_f32_e32 v36, v36, v37
	v_mov_b32_e32 v37, v36
	s_nop 1
	v_permlane32_swap_b32_e32 v36, v37
	v_add_f32_e32 v36, v36, v37
	global_load_dwordx4 v[44:47], v[72:73], off offset:1024
	global_load_dwordx4 v[48:51], v[72:73], off offset:2048
	global_load_dwordx4 v[52:55], v[72:73], off offset:3072
	global_load_dwordx4 v[56:59], v[82:83], off
	global_load_dwordx4 v[60:63], v[84:85], off
	global_load_dwordx4 v[64:67], v[86:87], off
	global_load_dwordx4 v[94:97], v[88:89], off
	v_fmamk_f32 v36, v36, 0x3a000000, v101
	v_mul_f32_e32 v37, 0x4f800000, v36
	v_cmp_gt_f32_e32 vcc, s22, v36
	s_nop 1
	v_cndmask_b32_e32 v36, v36, v37, vcc
	v_sqrt_f32_e32 v37, v36
	s_nop 0
	v_add_u32_e32 v38, -1, v37
	v_add_u32_e32 v39, 1, v37
	v_fma_f32 v40, -v38, v37, v36
	v_fma_f32 v41, -v39, v37, v36
	v_cmp_ge_f32_e64 s[0:1], 0, v40
	s_nop 1
	v_cndmask_b32_e64 v37, v37, v38, s[0:1]
	v_cmp_lt_f32_e64 s[0:1], 0, v41
	s_nop 1
	v_cndmask_b32_e64 v37, v37, v39, s[0:1]
	v_mul_f32_e32 v38, 0x37800000, v37
	v_cndmask_b32_e32 v37, v37, v38, vcc
	v_cmp_class_f32_e32 vcc, v36, v102
	s_nop 1
	v_cndmask_b32_e32 v36, v37, v36, vcc
	v_div_scale_f32 v37, s[0:1], v36, v36, 1.0
	v_rcp_f32_e32 v39, v37
	v_div_scale_f32 v38, vcc, 1.0, v36, 1.0
	v_fma_f32 v40, -v37, v39, 1.0
	v_fmac_f32_e32 v39, v40, v39
	v_mul_f32_e32 v40, v38, v39
	v_fma_f32 v41, -v37, v40, v38
	v_fmac_f32_e32 v40, v41, v39
	v_fma_f32 v37, -v37, v40, v38
	v_div_fmas_f32 v37, v37, v39, v40
	v_div_fixup_f32 v36, v37, v36, 1.0
	v_add_co_u32_e32 v38, vcc, s23, v92
	s_nop 1
	v_addc_co_u32_e32 v39, vcc, 0, v93, vcc
	s_waitcnt vmcnt(0)
	v_pk_mul_f32 v[0:1], v[0:1], v[36:37] op_sel_hi:[1,0]
	v_pk_mul_f32 v[2:3], v[2:3], v[36:37] op_sel_hi:[1,0]
	v_pk_mul_f32 v[0:1], v[28:29], v[0:1]
	v_pk_mul_f32 v[2:3], v[30:31], v[2:3]
	global_store_dwordx4 v[92:93], v[0:3], off
	v_pk_mul_f32 v[4:5], v[4:5], v[36:37] op_sel_hi:[1,0]
	v_pk_mul_f32 v[6:7], v[6:7], v[36:37] op_sel_hi:[1,0]
	v_pk_mul_f32 v[4:5], v[44:45], v[4:5]
	v_pk_mul_f32 v[6:7], v[46:47], v[6:7]
	global_store_dwordx4 v[92:93], v[4:7], off offset:1024
	v_pk_mul_f32 v[8:9], v[8:9], v[36:37] op_sel_hi:[1,0]
	v_pk_mul_f32 v[10:11], v[10:11], v[36:37] op_sel_hi:[1,0]
	v_pk_mul_f32 v[8:9], v[48:49], v[8:9]
	v_pk_mul_f32 v[10:11], v[50:51], v[10:11]
	global_store_dwordx4 v[92:93], v[8:11], off offset:2048
	v_pk_mul_f32 v[12:13], v[12:13], v[36:37] op_sel_hi:[1,0]
	v_pk_mul_f32 v[14:15], v[14:15], v[36:37] op_sel_hi:[1,0]
	v_pk_mul_f32 v[12:13], v[52:53], v[12:13]
	v_pk_mul_f32 v[14:15], v[54:55], v[14:15]
	global_store_dwordx4 v[92:93], v[12:15], off offset:3072
	v_pk_mul_f32 v[16:17], v[16:17], v[36:37] op_sel_hi:[1,0]
	v_pk_mul_f32 v[18:19], v[18:19], v[36:37] op_sel_hi:[1,0]
	v_pk_mul_f32 v[16:17], v[56:57], v[16:17]
	v_pk_mul_f32 v[18:19], v[58:59], v[18:19]
	global_store_dwordx4 v[38:39], v[16:19], off
	v_pk_mul_f32 v[20:21], v[20:21], v[36:37] op_sel_hi:[1,0]
	v_pk_mul_f32 v[22:23], v[22:23], v[36:37] op_sel_hi:[1,0]
	v_pk_mul_f32 v[20:21], v[60:61], v[20:21]
	v_pk_mul_f32 v[22:23], v[62:63], v[22:23]
	global_store_dwordx4 v[38:39], v[20:23], off offset:1024
	v_pk_mul_f32 v[24:25], v[24:25], v[36:37] op_sel_hi:[1,0]
	v_pk_mul_f32 v[26:27], v[26:27], v[36:37] op_sel_hi:[1,0]
	v_pk_mul_f32 v[24:25], v[64:65], v[24:25]
	v_pk_mul_f32 v[26:27], v[66:67], v[26:27]
	global_store_dwordx4 v[38:39], v[24:27], off offset:2048
	v_pk_mul_f32 v[32:33], v[32:33], v[36:37] op_sel_hi:[1,0]
	v_pk_mul_f32 v[34:35], v[34:35], v[36:37] op_sel_hi:[1,0]
	v_pk_mul_f32 v[32:33], v[94:95], v[32:33]
	v_pk_mul_f32 v[34:35], v[96:97], v[34:35]
	global_store_dwordx4 v[38:39], v[32:35], off offset:3072
	s_cbranch_scc1 .LBB0_4682
